# A/B on all GEMM K-loops: the mid-section s_setprio 0 / s_setprio 1 yield between the two groups of 8 MFMAs removed (MFMA wave keeps priority for all 16); on top of the attention static raise
# speedup vs baseline: 1.0044x; 1.0044x over previous
.LBB0_124:
	s_add_i32 s79, s56, 2
	s_add_u32 s58, s54, 0x80
	s_addc_u32 s57, s55, 0
	s_cmp_eq_u32 s70, s56
	s_cselect_b32 s57, s41, s57
	s_cselect_b32 s56, s40, s58
	s_cselect_b32 s59, s53, s78
	s_cselect_b32 s58, s52, s77
	s_add_i32 s80, 0, 0x10000
	s_add_i32 s81, 0, 0x14000
	v_add_u32_e32 v2, s80, v183
	v_add_u32_e32 v14, s81, v183
	ds_read_b128 v[18:21], v2
	ds_read_b128 v[22:25], v2 offset:1024
	ds_read_b128 v[26:29], v2 offset:2048
	ds_read_b128 v[30:33], v2 offset:3072
	ds_read_b128 v[2:5], v14
	ds_read_b128 v[6:9], v14 offset:1024
	ds_read_b128 v[10:13], v14 offset:2048
	ds_read_b128 v[14:17], v14 offset:3072
	v_lshl_add_u64 v[176:177], s[54:55], 0, v[164:165]
	s_add_i32 m0, s62, 0xc000
	ds_read_b128 v[168:171], v184
	ds_read_b128 v[172:175], v184 offset:1024
	ds_read_b128 v[186:189], v184 offset:2048
	ds_read_b128 v[190:193], v184 offset:3072
	ds_read_b128 v[194:197], v184 offset:4096
	ds_read_b128 v[198:201], v184 offset:5120
	ds_read_b128 v[202:205], v184 offset:6144
	ds_read_b128 v[206:209], v184 offset:7168
	global_load_lds_dwordx4 v[176:177], off
	v_lshl_add_u64 v[176:177], s[54:55], 0, v[166:167]
	s_add_i32 m0, s62, 0xe000
	s_nop 0
	global_load_lds_dwordx4 v[176:177], off
	s_waitcnt vmcnt(8)
	s_waitcnt lgkmcnt(0)
	s_barrier
	s_setprio 1
	s_waitcnt lgkmcnt(0)
	v_mfma_scale_f32_16x16x128_f8f6f4 v[154:157], v[18:25], v[168:175], v[154:157], v180, v180 op_sel_hi:[0,0,0]
	v_mfma_scale_f32_16x16x128_f8f6f4 v[158:161], v[26:33], v[168:175], v[158:161], v180, v180 op_sel_hi:[0,0,0]
	v_mfma_scale_f32_16x16x128_f8f6f4 v[142:145], v[18:25], v[186:193], v[142:145], v180, v180 op_sel_hi:[0,0,0]
	v_mfma_scale_f32_16x16x128_f8f6f4 v[138:141], v[26:33], v[186:193], v[138:141], v180, v180 op_sel_hi:[0,0,0]
	v_mfma_scale_f32_16x16x128_f8f6f4 v[126:129], v[18:25], v[194:201], v[126:129], v180, v180 op_sel_hi:[0,0,0]
	v_mfma_scale_f32_16x16x128_f8f6f4 v[122:125], v[26:33], v[194:201], v[122:125], v180, v180 op_sel_hi:[0,0,0]
	v_mfma_scale_f32_16x16x128_f8f6f4 v[110:113], v[18:25], v[202:209], v[110:113], v180, v180 op_sel_hi:[0,0,0]
	v_mfma_scale_f32_16x16x128_f8f6f4 v[106:109], v[26:33], v[202:209], v[106:109], v180, v180 op_sel_hi:[0,0,0]
	v_mfma_scale_f32_16x16x128_f8f6f4 v[150:153], v[2:9], v[168:175], v[150:153], v180, v180 op_sel_hi:[0,0,0]
	v_mfma_scale_f32_16x16x128_f8f6f4 v[146:149], v[10:17], v[168:175], v[146:149], v180, v180 op_sel_hi:[0,0,0]
	v_mfma_scale_f32_16x16x128_f8f6f4 v[134:137], v[2:9], v[186:193], v[134:137], v180, v180 op_sel_hi:[0,0,0]
	v_mfma_scale_f32_16x16x128_f8f6f4 v[130:133], v[10:17], v[186:193], v[130:133], v180, v180 op_sel_hi:[0,0,0]
	v_mfma_scale_f32_16x16x128_f8f6f4 v[118:121], v[2:9], v[194:201], v[118:121], v180, v180 op_sel_hi:[0,0,0]
	v_mfma_scale_f32_16x16x128_f8f6f4 v[114:117], v[10:17], v[194:201], v[114:117], v180, v180 op_sel_hi:[0,0,0]
	v_mfma_scale_f32_16x16x128_f8f6f4 v[102:105], v[2:9], v[202:209], v[102:105], v180, v180 op_sel_hi:[0,0,0]
	v_mfma_scale_f32_16x16x128_f8f6f4 v[98:101], v[10:17], v[202:209], v[98:101], v180, v180 op_sel_hi:[0,0,0]
	s_setprio 0
	s_barrier
	s_add_i32 s80, s80, s20
	v_lshl_add_u64 v[168:169], s[58:59], 0, v[0:1]
	s_mov_b32 m0, s80
	ds_read_b128 v[186:189], v184 offset:16384
	ds_read_b128 v[190:193], v184 offset:17408
	ds_read_b128 v[194:197], v184 offset:18432
	ds_read_b128 v[198:201], v184 offset:19456
	ds_read_b128 v[202:205], v184 offset:20480
	ds_read_b128 v[206:209], v184 offset:21504
	ds_read_b128 v[212:215], v184 offset:22528
	ds_read_b128 v[216:219], v184 offset:23552
	global_load_lds_dwordx4 v[168:169], off
	s_add_i32 m0, s80, 0x2000
	s_add_u32 s58, s58, s8
	s_addc_u32 s59, s59, s9
	v_lshl_add_u64 v[170:171], v[168:169], 0, s[6:7]
	v_lshl_add_u64 v[172:173], s[58:59], 0, v[0:1]
	s_add_i32 s58, s81, s20
	global_load_lds_dwordx4 v[170:171], off
	s_mov_b32 m0, s58
	v_lshl_add_u64 v[174:175], v[172:173], 0, s[6:7]
	global_load_lds_dwordx4 v[172:173], off
	s_add_i32 m0, s58, 0x2000
	v_lshl_add_u64 v[176:177], s[56:57], 0, v[162:163]
	global_load_lds_dwordx4 v[174:175], off
	s_mov_b32 m0, s62
	v_lshl_add_u64 v[178:179], v[176:177], 0, s[6:7]
	global_load_lds_dwordx4 v[176:177], off
	s_mov_b32 m0, s63
	s_nop 0
	global_load_lds_dwordx4 v[178:179], off
	s_waitcnt vmcnt(8)
	s_waitcnt lgkmcnt(0)
	s_barrier
	s_setprio 1
	s_waitcnt lgkmcnt(0)
	v_mfma_scale_f32_16x16x128_f8f6f4 v[94:97], v[18:25], v[186:193], v[94:97], v180, v180 op_sel_hi:[0,0,0]
	v_mfma_scale_f32_16x16x128_f8f6f4 v[90:93], v[26:33], v[186:193], v[90:93], v180, v180 op_sel_hi:[0,0,0]
	v_mfma_scale_f32_16x16x128_f8f6f4 v[78:81], v[18:25], v[194:201], v[78:81], v180, v180 op_sel_hi:[0,0,0]
	v_mfma_scale_f32_16x16x128_f8f6f4 v[74:77], v[26:33], v[194:201], v[74:77], v180, v180 op_sel_hi:[0,0,0]
	v_mfma_scale_f32_16x16x128_f8f6f4 v[62:65], v[18:25], v[202:209], v[62:65], v180, v180 op_sel_hi:[0,0,0]
	v_mfma_scale_f32_16x16x128_f8f6f4 v[58:61], v[26:33], v[202:209], v[58:61], v180, v180 op_sel_hi:[0,0,0]
	v_mfma_scale_f32_16x16x128_f8f6f4 v[46:49], v[18:25], v[212:219], v[46:49], v180, v180 op_sel_hi:[0,0,0]
	v_mfma_scale_f32_16x16x128_f8f6f4 v[42:45], v[26:33], v[212:219], v[42:45], v180, v180 op_sel_hi:[0,0,0]
	v_mfma_scale_f32_16x16x128_f8f6f4 v[86:89], v[2:9], v[186:193], v[86:89], v180, v180 op_sel_hi:[0,0,0]
	v_mfma_scale_f32_16x16x128_f8f6f4 v[82:85], v[10:17], v[186:193], v[82:85], v180, v180 op_sel_hi:[0,0,0]
	v_mfma_scale_f32_16x16x128_f8f6f4 v[70:73], v[2:9], v[194:201], v[70:73], v180, v180 op_sel_hi:[0,0,0]
	v_mfma_scale_f32_16x16x128_f8f6f4 v[66:69], v[10:17], v[194:201], v[66:69], v180, v180 op_sel_hi:[0,0,0]
	v_mfma_scale_f32_16x16x128_f8f6f4 v[54:57], v[2:9], v[202:209], v[54:57], v180, v180 op_sel_hi:[0,0,0]
	v_mfma_scale_f32_16x16x128_f8f6f4 v[50:53], v[10:17], v[202:209], v[50:53], v180, v180 op_sel_hi:[0,0,0]
	v_mfma_scale_f32_16x16x128_f8f6f4 v[38:41], v[2:9], v[212:219], v[38:41], v180, v180 op_sel_hi:[0,0,0]
	v_mfma_scale_f32_16x16x128_f8f6f4 v[34:37], v[10:17], v[212:219], v[34:37], v180, v180 op_sel_hi:[0,0,0]
	s_setprio 0
	s_barrier
	s_add_i32 s58, 0, 0x18000
	s_add_i32 s59, 0, 0x1c000
	v_add_u32_e32 v14, s58, v183
	v_add_u32_e32 v30, s59, v183
	ds_read_b128 v[2:5], v14
	ds_read_b128 v[6:9], v14 offset:1024
	ds_read_b128 v[10:13], v14 offset:2048
	ds_read_b128 v[14:17], v14 offset:3072
	ds_read_b128 v[18:21], v30
	ds_read_b128 v[22:25], v30 offset:1024
	ds_read_b128 v[26:29], v30 offset:2048
	ds_read_b128 v[30:33], v30 offset:3072
	s_add_u32 s56, s56, s8
	s_addc_u32 s57, s57, s9
	s_mov_b32 m0, s64
	v_lshl_add_u64 v[220:221], s[56:57], 0, v[162:163]
	ds_read_b128 v[186:189], v184 offset:32768
	ds_read_b128 v[190:193], v184 offset:33792
	ds_read_b128 v[194:197], v184 offset:34816
	ds_read_b128 v[198:201], v184 offset:35840
	ds_read_b128 v[202:205], v184 offset:36864
	ds_read_b128 v[206:209], v184 offset:37888
	ds_read_b128 v[212:215], v184 offset:38912
	ds_read_b128 v[216:219], v184 offset:39936
	global_load_lds_dwordx4 v[220:221], off
	v_lshl_add_u64 v[220:221], v[220:221], 0, s[6:7]
	s_mov_b32 m0, s65
	s_nop 0
	global_load_lds_dwordx4 v[220:221], off
	s_waitcnt vmcnt(8)
	s_waitcnt lgkmcnt(0)
	s_barrier
	s_setprio 1
	s_waitcnt lgkmcnt(0)
	v_mfma_scale_f32_16x16x128_f8f6f4 v[154:157], v[2:9], v[186:193], v[154:157], v180, v180 op_sel_hi:[0,0,0]
	v_mfma_scale_f32_16x16x128_f8f6f4 v[158:161], v[10:17], v[186:193], v[158:161], v180, v180 op_sel_hi:[0,0,0]
	v_mfma_scale_f32_16x16x128_f8f6f4 v[142:145], v[2:9], v[194:201], v[142:145], v180, v180 op_sel_hi:[0,0,0]
	v_mfma_scale_f32_16x16x128_f8f6f4 v[138:141], v[10:17], v[194:201], v[138:141], v180, v180 op_sel_hi:[0,0,0]
	v_mfma_scale_f32_16x16x128_f8f6f4 v[126:129], v[2:9], v[202:209], v[126:129], v180, v180 op_sel_hi:[0,0,0]
	v_mfma_scale_f32_16x16x128_f8f6f4 v[122:125], v[10:17], v[202:209], v[122:125], v180, v180 op_sel_hi:[0,0,0]
	v_mfma_scale_f32_16x16x128_f8f6f4 v[110:113], v[2:9], v[212:219], v[110:113], v180, v180 op_sel_hi:[0,0,0]
	v_mfma_scale_f32_16x16x128_f8f6f4 v[106:109], v[10:17], v[212:219], v[106:109], v180, v180 op_sel_hi:[0,0,0]
	v_mfma_scale_f32_16x16x128_f8f6f4 v[150:153], v[18:25], v[186:193], v[150:153], v180, v180 op_sel_hi:[0,0,0]
	v_mfma_scale_f32_16x16x128_f8f6f4 v[146:149], v[26:33], v[186:193], v[146:149], v180, v180 op_sel_hi:[0,0,0]
	v_mfma_scale_f32_16x16x128_f8f6f4 v[134:137], v[18:25], v[194:201], v[134:137], v180, v180 op_sel_hi:[0,0,0]
	v_mfma_scale_f32_16x16x128_f8f6f4 v[130:133], v[26:33], v[194:201], v[130:133], v180, v180 op_sel_hi:[0,0,0]
	v_mfma_scale_f32_16x16x128_f8f6f4 v[118:121], v[18:25], v[202:209], v[118:121], v180, v180 op_sel_hi:[0,0,0]
	v_mfma_scale_f32_16x16x128_f8f6f4 v[114:117], v[26:33], v[202:209], v[114:117], v180, v180 op_sel_hi:[0,0,0]
	v_mfma_scale_f32_16x16x128_f8f6f4 v[102:105], v[18:25], v[212:219], v[102:105], v180, v180 op_sel_hi:[0,0,0]
	v_mfma_scale_f32_16x16x128_f8f6f4 v[98:101], v[26:33], v[212:219], v[98:101], v180, v180 op_sel_hi:[0,0,0]
	s_setprio 0
	s_barrier
	s_add_i32 s56, s58, s20
	v_lshl_add_u64 v[168:169], v[168:169], 0, s[36:37]
	s_mov_b32 m0, s56
	ds_read_b128 v[186:189], v184 offset:49152
	ds_read_b128 v[190:193], v184 offset:50176
	ds_read_b128 v[194:197], v184 offset:51200
	ds_read_b128 v[198:201], v184 offset:52224
	ds_read_b128 v[202:205], v184 offset:53248
	ds_read_b128 v[206:209], v184 offset:54272
	ds_read_b128 v[212:215], v184 offset:55296
	ds_read_b128 v[216:219], v184 offset:56320
	global_load_lds_dwordx4 v[168:169], off
	v_lshl_add_u64 v[168:169], v[170:171], 0, s[36:37]
	s_add_i32 m0, s56, 0x2000
	s_add_i32 s56, s59, s20
	global_load_lds_dwordx4 v[168:169], off
	v_lshl_add_u64 v[168:169], v[172:173], 0, s[36:37]
	s_mov_b32 m0, s56
	s_nop 0
	global_load_lds_dwordx4 v[168:169], off
	v_lshl_add_u64 v[168:169], v[174:175], 0, s[36:37]
	s_add_i32 m0, s56, 0x2000
	s_nop 0
	global_load_lds_dwordx4 v[168:169], off
	v_lshl_add_u64 v[168:169], v[176:177], 0, s[36:37]
	s_mov_b32 m0, s66
	s_nop 0
	global_load_lds_dwordx4 v[168:169], off
	v_lshl_add_u64 v[168:169], v[178:179], 0, s[36:37]
	s_mov_b32 m0, s67
	s_nop 0
	global_load_lds_dwordx4 v[168:169], off
	s_waitcnt vmcnt(8)
	s_waitcnt lgkmcnt(0)
	s_barrier
	s_setprio 1
	s_waitcnt lgkmcnt(0)
	v_mfma_scale_f32_16x16x128_f8f6f4 v[94:97], v[2:9], v[186:193], v[94:97], v180, v180 op_sel_hi:[0,0,0]
	v_mfma_scale_f32_16x16x128_f8f6f4 v[90:93], v[10:17], v[186:193], v[90:93], v180, v180 op_sel_hi:[0,0,0]
	v_mfma_scale_f32_16x16x128_f8f6f4 v[78:81], v[2:9], v[194:201], v[78:81], v180, v180 op_sel_hi:[0,0,0]
	v_mfma_scale_f32_16x16x128_f8f6f4 v[74:77], v[10:17], v[194:201], v[74:77], v180, v180 op_sel_hi:[0,0,0]
	v_mfma_scale_f32_16x16x128_f8f6f4 v[62:65], v[2:9], v[202:209], v[62:65], v180, v180 op_sel_hi:[0,0,0]
	v_mfma_scale_f32_16x16x128_f8f6f4 v[58:61], v[10:17], v[202:209], v[58:61], v180, v180 op_sel_hi:[0,0,0]
	v_mfma_scale_f32_16x16x128_f8f6f4 v[46:49], v[2:9], v[212:219], v[46:49], v180, v180 op_sel_hi:[0,0,0]
	v_mfma_scale_f32_16x16x128_f8f6f4 v[42:45], v[10:17], v[212:219], v[42:45], v180, v180 op_sel_hi:[0,0,0]
	v_mfma_scale_f32_16x16x128_f8f6f4 v[86:89], v[18:25], v[186:193], v[86:89], v180, v180 op_sel_hi:[0,0,0]
	v_mfma_scale_f32_16x16x128_f8f6f4 v[82:85], v[26:33], v[186:193], v[82:85], v180, v180 op_sel_hi:[0,0,0]
	v_mfma_scale_f32_16x16x128_f8f6f4 v[70:73], v[18:25], v[194:201], v[70:73], v180, v180 op_sel_hi:[0,0,0]
	v_mfma_scale_f32_16x16x128_f8f6f4 v[66:69], v[26:33], v[194:201], v[66:69], v180, v180 op_sel_hi:[0,0,0]
	v_mfma_scale_f32_16x16x128_f8f6f4 v[54:57], v[18:25], v[202:209], v[54:57], v180, v180 op_sel_hi:[0,0,0]
	v_mfma_scale_f32_16x16x128_f8f6f4 v[50:53], v[26:33], v[202:209], v[50:53], v180, v180 op_sel_hi:[0,0,0]
	v_mfma_scale_f32_16x16x128_f8f6f4 v[38:41], v[18:25], v[212:219], v[38:41], v180, v180 op_sel_hi:[0,0,0]
	v_mfma_scale_f32_16x16x128_f8f6f4 v[34:37], v[26:33], v[212:219], v[34:37], v180, v180 op_sel_hi:[0,0,0]
	s_setprio 0
	s_barrier
	s_add_u32 s54, s54, 0x100
	s_addc_u32 s55, s55, 0
	s_add_u32 s77, s77, 0x100
	s_addc_u32 s78, s78, 0
	s_cmp_ge_i32 s79, s30
	s_mov_b32 s56, s79
	s_cbranch_scc0 .LBB0_124

.LBB0_145:
	s_add_i32 s79, s56, 2
	s_add_u32 s58, s54, 0x80
	s_addc_u32 s57, s55, 0
	s_cmp_eq_u32 s73, s56
	s_cselect_b32 s57, s41, s57
	s_cselect_b32 s56, s40, s58
	s_cselect_b32 s59, s53, s78
	s_cselect_b32 s58, s52, s70
	s_add_i32 s80, 0, 0x10000
	s_add_i32 s81, 0, 0x14000
	v_add_u32_e32 v2, s80, v182
	v_add_u32_e32 v14, s81, v182
	ds_read_b128 v[18:21], v2
	ds_read_b128 v[22:25], v2 offset:1024
	ds_read_b128 v[26:29], v2 offset:2048
	ds_read_b128 v[30:33], v2 offset:3072
	ds_read_b128 v[2:5], v14
	ds_read_b128 v[6:9], v14 offset:1024
	ds_read_b128 v[10:13], v14 offset:2048
	ds_read_b128 v[14:17], v14 offset:3072
	v_lshl_add_u64 v[176:177], s[54:55], 0, v[164:165]
	s_add_i32 m0, s64, 0xc000
	ds_read_b128 v[168:171], v183
	ds_read_b128 v[172:175], v183 offset:1024
	ds_read_b128 v[184:187], v183 offset:2048
	ds_read_b128 v[188:191], v183 offset:3072
	ds_read_b128 v[192:195], v183 offset:4096
	ds_read_b128 v[196:199], v183 offset:5120
	ds_read_b128 v[200:203], v183 offset:6144
	ds_read_b128 v[204:207], v183 offset:7168
	global_load_lds_dwordx4 v[176:177], off
	v_lshl_add_u64 v[176:177], s[54:55], 0, v[166:167]
	s_add_i32 m0, s64, 0xe000
	s_nop 0
	global_load_lds_dwordx4 v[176:177], off
	s_waitcnt vmcnt(8)
	s_waitcnt lgkmcnt(0)
	s_barrier
	s_setprio 1
	s_waitcnt lgkmcnt(0)
	v_mfma_scale_f32_16x16x128_f8f6f4 v[158:161], v[18:25], v[168:175], v[158:161], v180, v180 op_sel_hi:[0,0,0]
	v_mfma_scale_f32_16x16x128_f8f6f4 v[154:157], v[26:33], v[168:175], v[154:157], v180, v180 op_sel_hi:[0,0,0]
	v_mfma_scale_f32_16x16x128_f8f6f4 v[142:145], v[18:25], v[184:191], v[142:145], v180, v180 op_sel_hi:[0,0,0]
	v_mfma_scale_f32_16x16x128_f8f6f4 v[138:141], v[26:33], v[184:191], v[138:141], v180, v180 op_sel_hi:[0,0,0]
	v_mfma_scale_f32_16x16x128_f8f6f4 v[126:129], v[18:25], v[192:199], v[126:129], v180, v180 op_sel_hi:[0,0,0]
	v_mfma_scale_f32_16x16x128_f8f6f4 v[122:125], v[26:33], v[192:199], v[122:125], v180, v180 op_sel_hi:[0,0,0]
	v_mfma_scale_f32_16x16x128_f8f6f4 v[110:113], v[18:25], v[200:207], v[110:113], v180, v180 op_sel_hi:[0,0,0]
	v_mfma_scale_f32_16x16x128_f8f6f4 v[106:109], v[26:33], v[200:207], v[106:109], v180, v180 op_sel_hi:[0,0,0]
	v_mfma_scale_f32_16x16x128_f8f6f4 v[150:153], v[2:9], v[168:175], v[150:153], v180, v180 op_sel_hi:[0,0,0]
	v_mfma_scale_f32_16x16x128_f8f6f4 v[146:149], v[10:17], v[168:175], v[146:149], v180, v180 op_sel_hi:[0,0,0]
	v_mfma_scale_f32_16x16x128_f8f6f4 v[134:137], v[2:9], v[184:191], v[134:137], v180, v180 op_sel_hi:[0,0,0]
	v_mfma_scale_f32_16x16x128_f8f6f4 v[130:133], v[10:17], v[184:191], v[130:133], v180, v180 op_sel_hi:[0,0,0]
	v_mfma_scale_f32_16x16x128_f8f6f4 v[118:121], v[2:9], v[192:199], v[118:121], v180, v180 op_sel_hi:[0,0,0]
	v_mfma_scale_f32_16x16x128_f8f6f4 v[114:117], v[10:17], v[192:199], v[114:117], v180, v180 op_sel_hi:[0,0,0]
	v_mfma_scale_f32_16x16x128_f8f6f4 v[102:105], v[2:9], v[200:207], v[102:105], v180, v180 op_sel_hi:[0,0,0]
	v_mfma_scale_f32_16x16x128_f8f6f4 v[98:101], v[10:17], v[200:207], v[98:101], v180, v180 op_sel_hi:[0,0,0]
	s_setprio 0
	s_barrier
	s_add_i32 s80, s80, s62
	v_lshl_add_u64 v[168:169], s[58:59], 0, v[0:1]
	s_mov_b32 m0, s80
	ds_read_b128 v[184:187], v183 offset:16384
	ds_read_b128 v[188:191], v183 offset:17408
	ds_read_b128 v[192:195], v183 offset:18432
	ds_read_b128 v[196:199], v183 offset:19456
	ds_read_b128 v[200:203], v183 offset:20480
	ds_read_b128 v[204:207], v183 offset:21504
	ds_read_b128 v[212:215], v183 offset:22528
	ds_read_b128 v[216:219], v183 offset:23552
	global_load_lds_dwordx4 v[168:169], off
	s_add_i32 m0, s80, 0x2000
	s_add_u32 s58, s58, s8
	s_addc_u32 s59, s59, s9
	v_lshl_add_u64 v[170:171], v[168:169], 0, s[6:7]
	v_lshl_add_u64 v[172:173], s[58:59], 0, v[0:1]
	s_add_i32 s58, s81, s62
	global_load_lds_dwordx4 v[170:171], off
	s_mov_b32 m0, s58
	v_lshl_add_u64 v[174:175], v[172:173], 0, s[6:7]
	global_load_lds_dwordx4 v[172:173], off
	s_add_i32 m0, s58, 0x2000
	v_lshl_add_u64 v[176:177], s[56:57], 0, v[162:163]
	global_load_lds_dwordx4 v[174:175], off
	s_mov_b32 m0, s64
	v_lshl_add_u64 v[178:179], v[176:177], 0, s[10:11]
	global_load_lds_dwordx4 v[176:177], off
	s_mov_b32 m0, s65
	s_nop 0
	global_load_lds_dwordx4 v[178:179], off
	s_waitcnt vmcnt(8)
	s_waitcnt lgkmcnt(0)
	s_barrier
	s_setprio 1
	s_waitcnt lgkmcnt(0)
	v_mfma_scale_f32_16x16x128_f8f6f4 v[94:97], v[18:25], v[184:191], v[94:97], v180, v180 op_sel_hi:[0,0,0]
	v_mfma_scale_f32_16x16x128_f8f6f4 v[90:93], v[26:33], v[184:191], v[90:93], v180, v180 op_sel_hi:[0,0,0]
	v_mfma_scale_f32_16x16x128_f8f6f4 v[78:81], v[18:25], v[192:199], v[78:81], v180, v180 op_sel_hi:[0,0,0]
	v_mfma_scale_f32_16x16x128_f8f6f4 v[74:77], v[26:33], v[192:199], v[74:77], v180, v180 op_sel_hi:[0,0,0]
	v_mfma_scale_f32_16x16x128_f8f6f4 v[62:65], v[18:25], v[200:207], v[62:65], v180, v180 op_sel_hi:[0,0,0]
	v_mfma_scale_f32_16x16x128_f8f6f4 v[58:61], v[26:33], v[200:207], v[58:61], v180, v180 op_sel_hi:[0,0,0]
	v_mfma_scale_f32_16x16x128_f8f6f4 v[46:49], v[18:25], v[212:219], v[46:49], v180, v180 op_sel_hi:[0,0,0]
	v_mfma_scale_f32_16x16x128_f8f6f4 v[42:45], v[26:33], v[212:219], v[42:45], v180, v180 op_sel_hi:[0,0,0]
	v_mfma_scale_f32_16x16x128_f8f6f4 v[86:89], v[2:9], v[184:191], v[86:89], v180, v180 op_sel_hi:[0,0,0]
	v_mfma_scale_f32_16x16x128_f8f6f4 v[82:85], v[10:17], v[184:191], v[82:85], v180, v180 op_sel_hi:[0,0,0]
	v_mfma_scale_f32_16x16x128_f8f6f4 v[70:73], v[2:9], v[192:199], v[70:73], v180, v180 op_sel_hi:[0,0,0]
	v_mfma_scale_f32_16x16x128_f8f6f4 v[66:69], v[10:17], v[192:199], v[66:69], v180, v180 op_sel_hi:[0,0,0]
	v_mfma_scale_f32_16x16x128_f8f6f4 v[54:57], v[2:9], v[200:207], v[54:57], v180, v180 op_sel_hi:[0,0,0]
	v_mfma_scale_f32_16x16x128_f8f6f4 v[50:53], v[10:17], v[200:207], v[50:53], v180, v180 op_sel_hi:[0,0,0]
	v_mfma_scale_f32_16x16x128_f8f6f4 v[38:41], v[2:9], v[212:219], v[38:41], v180, v180 op_sel_hi:[0,0,0]
	v_mfma_scale_f32_16x16x128_f8f6f4 v[34:37], v[10:17], v[212:219], v[34:37], v180, v180 op_sel_hi:[0,0,0]
	s_setprio 0
	s_barrier
	s_add_i32 s58, 0, 0x18000
	s_add_i32 s59, 0, 0x1c000
	v_add_u32_e32 v14, s58, v182
	v_add_u32_e32 v30, s59, v182
	ds_read_b128 v[2:5], v14
	ds_read_b128 v[6:9], v14 offset:1024
	ds_read_b128 v[10:13], v14 offset:2048
	ds_read_b128 v[14:17], v14 offset:3072
	ds_read_b128 v[18:21], v30
	ds_read_b128 v[22:25], v30 offset:1024
	ds_read_b128 v[26:29], v30 offset:2048
	ds_read_b128 v[30:33], v30 offset:3072
	s_add_u32 s56, s56, s6
	s_addc_u32 s57, s57, s7
	s_mov_b32 m0, s66
	v_lshl_add_u64 v[208:209], s[56:57], 0, v[162:163]
	ds_read_b128 v[184:187], v183 offset:32768
	ds_read_b128 v[188:191], v183 offset:33792
	ds_read_b128 v[192:195], v183 offset:34816
	ds_read_b128 v[196:199], v183 offset:35840
	ds_read_b128 v[200:203], v183 offset:36864
	ds_read_b128 v[204:207], v183 offset:37888
	ds_read_b128 v[212:215], v183 offset:38912
	ds_read_b128 v[216:219], v183 offset:39936
	global_load_lds_dwordx4 v[208:209], off
	v_lshl_add_u64 v[208:209], v[208:209], 0, s[10:11]
	s_mov_b32 m0, s67
	s_nop 0
	global_load_lds_dwordx4 v[208:209], off
	s_waitcnt vmcnt(8)
	s_waitcnt lgkmcnt(0)
	s_barrier
	s_setprio 1
	s_waitcnt lgkmcnt(0)
	v_mfma_scale_f32_16x16x128_f8f6f4 v[158:161], v[2:9], v[184:191], v[158:161], v180, v180 op_sel_hi:[0,0,0]
	v_mfma_scale_f32_16x16x128_f8f6f4 v[154:157], v[10:17], v[184:191], v[154:157], v180, v180 op_sel_hi:[0,0,0]
	v_mfma_scale_f32_16x16x128_f8f6f4 v[142:145], v[2:9], v[192:199], v[142:145], v180, v180 op_sel_hi:[0,0,0]
	v_mfma_scale_f32_16x16x128_f8f6f4 v[138:141], v[10:17], v[192:199], v[138:141], v180, v180 op_sel_hi:[0,0,0]
	v_mfma_scale_f32_16x16x128_f8f6f4 v[126:129], v[2:9], v[200:207], v[126:129], v180, v180 op_sel_hi:[0,0,0]
	v_mfma_scale_f32_16x16x128_f8f6f4 v[122:125], v[10:17], v[200:207], v[122:125], v180, v180 op_sel_hi:[0,0,0]
	v_mfma_scale_f32_16x16x128_f8f6f4 v[110:113], v[2:9], v[212:219], v[110:113], v180, v180 op_sel_hi:[0,0,0]
	v_mfma_scale_f32_16x16x128_f8f6f4 v[106:109], v[10:17], v[212:219], v[106:109], v180, v180 op_sel_hi:[0,0,0]
	v_mfma_scale_f32_16x16x128_f8f6f4 v[150:153], v[18:25], v[184:191], v[150:153], v180, v180 op_sel_hi:[0,0,0]
	v_mfma_scale_f32_16x16x128_f8f6f4 v[146:149], v[26:33], v[184:191], v[146:149], v180, v180 op_sel_hi:[0,0,0]
	v_mfma_scale_f32_16x16x128_f8f6f4 v[134:137], v[18:25], v[192:199], v[134:137], v180, v180 op_sel_hi:[0,0,0]
	v_mfma_scale_f32_16x16x128_f8f6f4 v[130:133], v[26:33], v[192:199], v[130:133], v180, v180 op_sel_hi:[0,0,0]
	v_mfma_scale_f32_16x16x128_f8f6f4 v[118:121], v[18:25], v[200:207], v[118:121], v180, v180 op_sel_hi:[0,0,0]
	v_mfma_scale_f32_16x16x128_f8f6f4 v[114:117], v[26:33], v[200:207], v[114:117], v180, v180 op_sel_hi:[0,0,0]
	v_mfma_scale_f32_16x16x128_f8f6f4 v[102:105], v[18:25], v[212:219], v[102:105], v180, v180 op_sel_hi:[0,0,0]
	v_mfma_scale_f32_16x16x128_f8f6f4 v[98:101], v[26:33], v[212:219], v[98:101], v180, v180 op_sel_hi:[0,0,0]
	s_setprio 0
	s_barrier
	s_add_i32 s56, s58, s62
	v_lshl_add_u64 v[168:169], v[168:169], 0, s[36:37]
	s_mov_b32 m0, s56
	ds_read_b128 v[184:187], v183 offset:49152
	ds_read_b128 v[188:191], v183 offset:50176
	ds_read_b128 v[192:195], v183 offset:51200
	ds_read_b128 v[196:199], v183 offset:52224
	ds_read_b128 v[200:203], v183 offset:53248
	ds_read_b128 v[204:207], v183 offset:54272
	ds_read_b128 v[212:215], v183 offset:55296
	ds_read_b128 v[216:219], v183 offset:56320
	global_load_lds_dwordx4 v[168:169], off
	v_lshl_add_u64 v[168:169], v[170:171], 0, s[36:37]
	s_add_i32 m0, s56, 0x2000
	s_add_i32 s56, s59, s62
	global_load_lds_dwordx4 v[168:169], off
	v_lshl_add_u64 v[168:169], v[172:173], 0, s[36:37]
	s_mov_b32 m0, s56
	s_nop 0
	global_load_lds_dwordx4 v[168:169], off
	v_lshl_add_u64 v[168:169], v[174:175], 0, s[36:37]
	s_add_i32 m0, s56, 0x2000
	s_nop 0
	global_load_lds_dwordx4 v[168:169], off
	v_lshl_add_u64 v[168:169], v[176:177], 0, s[36:37]
	s_mov_b32 m0, s69
	s_nop 0
	global_load_lds_dwordx4 v[168:169], off
	v_lshl_add_u64 v[168:169], v[178:179], 0, s[36:37]
	s_mov_b32 m0, s72
	s_nop 0
	global_load_lds_dwordx4 v[168:169], off
	s_waitcnt vmcnt(8)
	s_waitcnt lgkmcnt(0)
	s_barrier
	s_setprio 1
	s_waitcnt lgkmcnt(0)
	v_mfma_scale_f32_16x16x128_f8f6f4 v[94:97], v[2:9], v[184:191], v[94:97], v180, v180 op_sel_hi:[0,0,0]
	v_mfma_scale_f32_16x16x128_f8f6f4 v[90:93], v[10:17], v[184:191], v[90:93], v180, v180 op_sel_hi:[0,0,0]
	v_mfma_scale_f32_16x16x128_f8f6f4 v[78:81], v[2:9], v[192:199], v[78:81], v180, v180 op_sel_hi:[0,0,0]
	v_mfma_scale_f32_16x16x128_f8f6f4 v[74:77], v[10:17], v[192:199], v[74:77], v180, v180 op_sel_hi:[0,0,0]
	v_mfma_scale_f32_16x16x128_f8f6f4 v[62:65], v[2:9], v[200:207], v[62:65], v180, v180 op_sel_hi:[0,0,0]
	v_mfma_scale_f32_16x16x128_f8f6f4 v[58:61], v[10:17], v[200:207], v[58:61], v180, v180 op_sel_hi:[0,0,0]
	v_mfma_scale_f32_16x16x128_f8f6f4 v[46:49], v[2:9], v[212:219], v[46:49], v180, v180 op_sel_hi:[0,0,0]
	v_mfma_scale_f32_16x16x128_f8f6f4 v[42:45], v[10:17], v[212:219], v[42:45], v180, v180 op_sel_hi:[0,0,0]
	v_mfma_scale_f32_16x16x128_f8f6f4 v[86:89], v[18:25], v[184:191], v[86:89], v180, v180 op_sel_hi:[0,0,0]
	v_mfma_scale_f32_16x16x128_f8f6f4 v[82:85], v[26:33], v[184:191], v[82:85], v180, v180 op_sel_hi:[0,0,0]
	v_mfma_scale_f32_16x16x128_f8f6f4 v[70:73], v[18:25], v[192:199], v[70:73], v180, v180 op_sel_hi:[0,0,0]
	v_mfma_scale_f32_16x16x128_f8f6f4 v[66:69], v[26:33], v[192:199], v[66:69], v180, v180 op_sel_hi:[0,0,0]
	v_mfma_scale_f32_16x16x128_f8f6f4 v[54:57], v[18:25], v[200:207], v[54:57], v180, v180 op_sel_hi:[0,0,0]
	v_mfma_scale_f32_16x16x128_f8f6f4 v[50:53], v[26:33], v[200:207], v[50:53], v180, v180 op_sel_hi:[0,0,0]
	v_mfma_scale_f32_16x16x128_f8f6f4 v[38:41], v[18:25], v[212:219], v[38:41], v180, v180 op_sel_hi:[0,0,0]
	v_mfma_scale_f32_16x16x128_f8f6f4 v[34:37], v[26:33], v[212:219], v[34:37], v180, v180 op_sel_hi:[0,0,0]
	s_setprio 0
	s_barrier
	s_add_u32 s54, s54, 0x100
	s_addc_u32 s55, s55, 0
	s_add_u32 s70, s70, 0x100
	s_addc_u32 s78, s78, 0
	s_cmp_ge_i32 s79, s30
	s_mov_b32 s56, s79
	s_cbranch_scc0 .LBB0_145
	v_readlane_b32 s70, v254, 49

.LBB0_735:
	s_add_i32 s20, s30, -1
	s_lshl_b64 s[60:61], s[30:31], 7
	s_add_u32 s12, s58, s60
	s_addc_u32 s18, s59, s61
	s_add_u32 s62, s56, s60
	s_addc_u32 s63, s57, s61
	s_cmp_eq_u32 s76, s30
	s_cselect_b32 s61, s41, s18
	s_cselect_b32 s60, s40, s12
	s_cselect_b32 s63, s55, s63
	s_cselect_b32 s62, s54, s62
	s_add_i32 s12, 0, 0x10000
	v_add_u32_e32 v0, s12, v167
	s_add_i32 s18, 0, 0x14000
	ds_read_b128 v[2:5], v0
	ds_read_b128 v[6:9], v0 offset:1024
	ds_read_b128 v[10:13], v0 offset:2048
	ds_read_b128 v[14:17], v0 offset:3072
	v_add_u32_e32 v0, s18, v167
	ds_read_b128 v[172:175], v0
	ds_read_b128 v[176:179], v0 offset:1024
	ds_read_b128 v[180:183], v0 offset:2048
	ds_read_b128 v[184:187], v0 offset:3072
	s_mov_b32 s21, s31
	s_lshl_b64 s[20:21], s[20:21], 7
	v_lshl_add_u64 v[160:161], v[150:151], 0, s[20:21]
	s_add_i32 m0, s72, 0xc000
	ds_read_b128 v[152:155], v169
	ds_read_b128 v[156:159], v169 offset:1024
	ds_read_b128 v[188:191], v169 offset:2048
	ds_read_b128 v[192:195], v169 offset:3072
	ds_read_b128 v[196:199], v169 offset:4096
	ds_read_b128 v[200:203], v169 offset:5120
	ds_read_b128 v[212:215], v169 offset:6144
	ds_read_b128 v[216:219], v169 offset:7168
	global_load_lds_dwordx4 v[160:161], off
	v_lshl_add_u64 v[160:161], v[160:161], 0, s[10:11]
	s_add_i32 m0, s72, 0xe000
	s_nop 0
	global_load_lds_dwordx4 v[160:161], off
	s_waitcnt vmcnt(8)
	s_waitcnt lgkmcnt(0)
	s_barrier
	s_setprio 1
	s_waitcnt lgkmcnt(0)
	v_mfma_scale_f32_16x16x128_f8f6f4 v[142:145], v[2:9], v[152:159], v[142:145], v164, v164 op_sel_hi:[0,0,0]
	v_mfma_scale_f32_16x16x128_f8f6f4 v[138:141], v[10:17], v[152:159], v[138:141], v164, v164 op_sel_hi:[0,0,0]
	v_mfma_scale_f32_16x16x128_f8f6f4 v[126:129], v[2:9], v[188:195], v[126:129], v164, v164 op_sel_hi:[0,0,0]
	v_mfma_scale_f32_16x16x128_f8f6f4 v[122:125], v[10:17], v[188:195], v[122:125], v164, v164 op_sel_hi:[0,0,0]
	v_mfma_scale_f32_16x16x128_f8f6f4 v[110:113], v[2:9], v[196:203], v[110:113], v164, v164 op_sel_hi:[0,0,0]
	v_mfma_scale_f32_16x16x128_f8f6f4 v[106:109], v[10:17], v[196:203], v[106:109], v164, v164 op_sel_hi:[0,0,0]
	v_mfma_scale_f32_16x16x128_f8f6f4 v[94:97], v[2:9], v[212:219], v[94:97], v164, v164 op_sel_hi:[0,0,0]
	v_mfma_scale_f32_16x16x128_f8f6f4 v[90:93], v[10:17], v[212:219], v[90:93], v164, v164 op_sel_hi:[0,0,0]
	v_mfma_scale_f32_16x16x128_f8f6f4 v[134:137], v[172:179], v[152:159], v[134:137], v164, v164 op_sel_hi:[0,0,0]
	v_mfma_scale_f32_16x16x128_f8f6f4 v[130:133], v[180:187], v[152:159], v[130:133], v164, v164 op_sel_hi:[0,0,0]
	v_mfma_scale_f32_16x16x128_f8f6f4 v[118:121], v[172:179], v[188:195], v[118:121], v164, v164 op_sel_hi:[0,0,0]
	v_mfma_scale_f32_16x16x128_f8f6f4 v[114:117], v[180:187], v[188:195], v[114:117], v164, v164 op_sel_hi:[0,0,0]
	v_mfma_scale_f32_16x16x128_f8f6f4 v[102:105], v[172:179], v[196:203], v[102:105], v164, v164 op_sel_hi:[0,0,0]
	v_mfma_scale_f32_16x16x128_f8f6f4 v[98:101], v[180:187], v[196:203], v[98:101], v164, v164 op_sel_hi:[0,0,0]
	v_mfma_scale_f32_16x16x128_f8f6f4 v[86:89], v[172:179], v[212:219], v[86:89], v164, v164 op_sel_hi:[0,0,0]
	v_mfma_scale_f32_16x16x128_f8f6f4 v[82:85], v[180:187], v[212:219], v[82:85], v164, v164 op_sel_hi:[0,0,0]
	s_setprio 0
	s_barrier
	s_add_i32 s12, s12, s69
	v_lshl_add_u64 v[152:153], s[62:63], 0, v[146:147]
	s_mov_b32 m0, s12
	ds_read_b128 v[188:191], v169 offset:16384
	ds_read_b128 v[192:195], v169 offset:17408
	ds_read_b128 v[196:199], v169 offset:18432
	ds_read_b128 v[200:203], v169 offset:19456
	ds_read_b128 v[212:215], v169 offset:20480
	ds_read_b128 v[216:219], v169 offset:21504
	ds_read_b128 v[240:243], v169 offset:22528
	ds_read_b128 v[244:247], v169 offset:23552
	global_load_lds_dwordx4 v[152:153], off
	s_add_i32 m0, s12, 0x2000
	s_add_u32 s20, s62, s8
	v_lshl_add_u64 v[154:155], v[152:153], 0, s[6:7]
	s_addc_u32 s21, s63, s9
	s_add_i32 s12, s18, s69
	global_load_lds_dwordx4 v[154:155], off
	v_lshl_add_u64 v[156:157], s[20:21], 0, v[146:147]
	s_mov_b32 m0, s12
	v_lshl_add_u64 v[158:159], v[156:157], 0, s[6:7]
	global_load_lds_dwordx4 v[156:157], off
	s_add_i32 m0, s12, 0x2000
	v_lshl_add_u64 v[160:161], s[60:61], 0, v[148:149]
	global_load_lds_dwordx4 v[158:159], off
	s_mov_b32 m0, s72
	v_lshl_add_u64 v[162:163], v[160:161], 0, s[10:11]
	global_load_lds_dwordx4 v[160:161], off
	s_mov_b32 m0, s73
	s_nop 0
	global_load_lds_dwordx4 v[162:163], off
	s_waitcnt vmcnt(8)
	s_waitcnt lgkmcnt(0)
	s_barrier
	s_setprio 1
	s_waitcnt lgkmcnt(0)
	v_mfma_scale_f32_16x16x128_f8f6f4 v[78:81], v[2:9], v[188:195], v[78:81], v164, v164 op_sel_hi:[0,0,0]
	v_mfma_scale_f32_16x16x128_f8f6f4 v[74:77], v[10:17], v[188:195], v[74:77], v164, v164 op_sel_hi:[0,0,0]
	v_mfma_scale_f32_16x16x128_f8f6f4 v[62:65], v[2:9], v[196:203], v[62:65], v164, v164 op_sel_hi:[0,0,0]
	v_mfma_scale_f32_16x16x128_f8f6f4 v[58:61], v[10:17], v[196:203], v[58:61], v164, v164 op_sel_hi:[0,0,0]
	v_mfma_scale_f32_16x16x128_f8f6f4 v[46:49], v[2:9], v[212:219], v[46:49], v164, v164 op_sel_hi:[0,0,0]
	v_mfma_scale_f32_16x16x128_f8f6f4 v[42:45], v[10:17], v[212:219], v[42:45], v164, v164 op_sel_hi:[0,0,0]
	v_mfma_scale_f32_16x16x128_f8f6f4 v[30:33], v[2:9], v[240:247], v[30:33], v164, v164 op_sel_hi:[0,0,0]
	v_mfma_scale_f32_16x16x128_f8f6f4 v[26:29], v[10:17], v[240:247], v[26:29], v164, v164 op_sel_hi:[0,0,0]
	v_mfma_scale_f32_16x16x128_f8f6f4 v[70:73], v[172:179], v[188:195], v[70:73], v164, v164 op_sel_hi:[0,0,0]
	v_mfma_scale_f32_16x16x128_f8f6f4 v[66:69], v[180:187], v[188:195], v[66:69], v164, v164 op_sel_hi:[0,0,0]
	v_mfma_scale_f32_16x16x128_f8f6f4 v[54:57], v[172:179], v[196:203], v[54:57], v164, v164 op_sel_hi:[0,0,0]
	v_mfma_scale_f32_16x16x128_f8f6f4 v[50:53], v[180:187], v[196:203], v[50:53], v164, v164 op_sel_hi:[0,0,0]
	v_mfma_scale_f32_16x16x128_f8f6f4 v[38:41], v[172:179], v[212:219], v[38:41], v164, v164 op_sel_hi:[0,0,0]
	v_mfma_scale_f32_16x16x128_f8f6f4 v[34:37], v[180:187], v[212:219], v[34:37], v164, v164 op_sel_hi:[0,0,0]
	v_mfma_scale_f32_16x16x128_f8f6f4 v[22:25], v[172:179], v[240:247], v[22:25], v164, v164 op_sel_hi:[0,0,0]
	v_mfma_scale_f32_16x16x128_f8f6f4 v[18:21], v[180:187], v[240:247], v[18:21], v164, v164 op_sel_hi:[0,0,0]
	s_setprio 0
	s_barrier
	s_add_i32 s12, 0, 0x18000
	v_add_u32_e32 v0, s12, v167
	s_add_i32 s18, 0, 0x1c000
	ds_read_b128 v[10:13], v0
	ds_read_b128 v[14:17], v0 offset:1024
	ds_read_b128 v[172:175], v0 offset:2048
	ds_read_b128 v[176:179], v0 offset:3072
	v_add_u32_e32 v0, s18, v167
	ds_read_b128 v[2:5], v0
	ds_read_b128 v[6:9], v0 offset:1024
	ds_read_b128 v[180:183], v0 offset:2048
	ds_read_b128 v[184:187], v0 offset:3072
	s_add_u32 s20, s60, s6
	s_addc_u32 s21, s61, s7
	s_mov_b32 m0, s74
	v_lshl_add_u64 v[204:205], s[20:21], 0, v[148:149]
	ds_read_b128 v[188:191], v169 offset:32768
	ds_read_b128 v[192:195], v169 offset:33792
	ds_read_b128 v[196:199], v169 offset:34816
	ds_read_b128 v[200:203], v169 offset:35840
	ds_read_b128 v[212:215], v169 offset:36864
	ds_read_b128 v[216:219], v169 offset:37888
	ds_read_b128 v[240:243], v169 offset:38912
	ds_read_b128 v[244:247], v169 offset:39936
	global_load_lds_dwordx4 v[204:205], off
	v_lshl_add_u64 v[204:205], v[204:205], 0, s[10:11]
	s_mov_b32 m0, s75
	s_nop 0
	global_load_lds_dwordx4 v[204:205], off
	s_waitcnt vmcnt(8)
	s_waitcnt lgkmcnt(0)
	s_barrier
	s_setprio 1
	s_waitcnt lgkmcnt(0)
	v_mfma_scale_f32_16x16x128_f8f6f4 v[142:145], v[10:17], v[188:195], v[142:145], v164, v164 op_sel_hi:[0,0,0]
	v_mfma_scale_f32_16x16x128_f8f6f4 v[138:141], v[172:179], v[188:195], v[138:141], v164, v164 op_sel_hi:[0,0,0]
	v_mfma_scale_f32_16x16x128_f8f6f4 v[126:129], v[10:17], v[196:203], v[126:129], v164, v164 op_sel_hi:[0,0,0]
	v_mfma_scale_f32_16x16x128_f8f6f4 v[122:125], v[172:179], v[196:203], v[122:125], v164, v164 op_sel_hi:[0,0,0]
	v_mfma_scale_f32_16x16x128_f8f6f4 v[110:113], v[10:17], v[212:219], v[110:113], v164, v164 op_sel_hi:[0,0,0]
	v_mfma_scale_f32_16x16x128_f8f6f4 v[106:109], v[172:179], v[212:219], v[106:109], v164, v164 op_sel_hi:[0,0,0]
	v_mfma_scale_f32_16x16x128_f8f6f4 v[94:97], v[10:17], v[240:247], v[94:97], v164, v164 op_sel_hi:[0,0,0]
	v_mfma_scale_f32_16x16x128_f8f6f4 v[90:93], v[172:179], v[240:247], v[90:93], v164, v164 op_sel_hi:[0,0,0]
	v_mfma_scale_f32_16x16x128_f8f6f4 v[134:137], v[2:9], v[188:195], v[134:137], v164, v164 op_sel_hi:[0,0,0]
	v_mfma_scale_f32_16x16x128_f8f6f4 v[130:133], v[180:187], v[188:195], v[130:133], v164, v164 op_sel_hi:[0,0,0]
	v_mfma_scale_f32_16x16x128_f8f6f4 v[118:121], v[2:9], v[196:203], v[118:121], v164, v164 op_sel_hi:[0,0,0]
	v_mfma_scale_f32_16x16x128_f8f6f4 v[114:117], v[180:187], v[196:203], v[114:117], v164, v164 op_sel_hi:[0,0,0]
	v_mfma_scale_f32_16x16x128_f8f6f4 v[102:105], v[2:9], v[212:219], v[102:105], v164, v164 op_sel_hi:[0,0,0]
	v_mfma_scale_f32_16x16x128_f8f6f4 v[98:101], v[180:187], v[212:219], v[98:101], v164, v164 op_sel_hi:[0,0,0]
	v_mfma_scale_f32_16x16x128_f8f6f4 v[86:89], v[2:9], v[240:247], v[86:89], v164, v164 op_sel_hi:[0,0,0]
	v_mfma_scale_f32_16x16x128_f8f6f4 v[82:85], v[180:187], v[240:247], v[82:85], v164, v164 op_sel_hi:[0,0,0]
	s_setprio 0
	s_barrier
	s_add_i32 s12, s12, s69
	v_lshl_add_u64 v[152:153], v[152:153], 0, s[36:37]
	s_mov_b32 m0, s12
	ds_read_b128 v[188:191], v169 offset:49152
	ds_read_b128 v[192:195], v169 offset:50176
	ds_read_b128 v[196:199], v169 offset:51200
	ds_read_b128 v[200:203], v169 offset:52224
	ds_read_b128 v[212:215], v169 offset:53248
	ds_read_b128 v[216:219], v169 offset:54272
	ds_read_b128 v[240:243], v169 offset:55296
	ds_read_b128 v[244:247], v169 offset:56320
	global_load_lds_dwordx4 v[152:153], off
	v_lshl_add_u64 v[152:153], v[154:155], 0, s[36:37]
	s_add_i32 m0, s12, 0x2000
	s_add_i32 s12, s18, s69
	global_load_lds_dwordx4 v[152:153], off
	v_lshl_add_u64 v[152:153], v[156:157], 0, s[36:37]
	s_mov_b32 m0, s12
	s_nop 0
	global_load_lds_dwordx4 v[152:153], off
	v_lshl_add_u64 v[152:153], v[158:159], 0, s[36:37]
	s_add_i32 m0, s12, 0x2000
	s_nop 0
	global_load_lds_dwordx4 v[152:153], off
	v_lshl_add_u64 v[152:153], v[160:161], 0, s[36:37]
	s_mov_b32 m0, s78
	s_nop 0
	global_load_lds_dwordx4 v[152:153], off
	v_lshl_add_u64 v[152:153], v[162:163], 0, s[36:37]
	s_mov_b32 m0, s79
	s_nop 0
	global_load_lds_dwordx4 v[152:153], off
	s_waitcnt vmcnt(8)
	s_waitcnt lgkmcnt(0)
	s_barrier
	s_setprio 1
	s_waitcnt lgkmcnt(0)
	v_mfma_scale_f32_16x16x128_f8f6f4 v[78:81], v[10:17], v[188:195], v[78:81], v164, v164 op_sel_hi:[0,0,0]
	v_mfma_scale_f32_16x16x128_f8f6f4 v[74:77], v[172:179], v[188:195], v[74:77], v164, v164 op_sel_hi:[0,0,0]
	v_mfma_scale_f32_16x16x128_f8f6f4 v[62:65], v[10:17], v[196:203], v[62:65], v164, v164 op_sel_hi:[0,0,0]
	v_mfma_scale_f32_16x16x128_f8f6f4 v[58:61], v[172:179], v[196:203], v[58:61], v164, v164 op_sel_hi:[0,0,0]
	v_mfma_scale_f32_16x16x128_f8f6f4 v[46:49], v[10:17], v[212:219], v[46:49], v164, v164 op_sel_hi:[0,0,0]
	v_mfma_scale_f32_16x16x128_f8f6f4 v[42:45], v[172:179], v[212:219], v[42:45], v164, v164 op_sel_hi:[0,0,0]
	v_mfma_scale_f32_16x16x128_f8f6f4 v[30:33], v[10:17], v[240:247], v[30:33], v164, v164 op_sel_hi:[0,0,0]
	v_mfma_scale_f32_16x16x128_f8f6f4 v[26:29], v[172:179], v[240:247], v[26:29], v164, v164 op_sel_hi:[0,0,0]
	v_mfma_scale_f32_16x16x128_f8f6f4 v[70:73], v[2:9], v[188:195], v[70:73], v164, v164 op_sel_hi:[0,0,0]
	v_mfma_scale_f32_16x16x128_f8f6f4 v[66:69], v[180:187], v[188:195], v[66:69], v164, v164 op_sel_hi:[0,0,0]
	v_mfma_scale_f32_16x16x128_f8f6f4 v[54:57], v[2:9], v[196:203], v[54:57], v164, v164 op_sel_hi:[0,0,0]
	v_mfma_scale_f32_16x16x128_f8f6f4 v[50:53], v[180:187], v[196:203], v[50:53], v164, v164 op_sel_hi:[0,0,0]
	v_mfma_scale_f32_16x16x128_f8f6f4 v[38:41], v[2:9], v[212:219], v[38:41], v164, v164 op_sel_hi:[0,0,0]
	v_mfma_scale_f32_16x16x128_f8f6f4 v[34:37], v[180:187], v[212:219], v[34:37], v164, v164 op_sel_hi:[0,0,0]
	v_mfma_scale_f32_16x16x128_f8f6f4 v[22:25], v[2:9], v[240:247], v[22:25], v164, v164 op_sel_hi:[0,0,0]
	v_mfma_scale_f32_16x16x128_f8f6f4 v[18:21], v[180:187], v[240:247], v[18:21], v164, v164 op_sel_hi:[0,0,0]
	s_setprio 0
	s_barrier
	s_add_i32 s12, s30, 2
	s_mul_i32 s18, s88, s80
	s_cmp_ge_i32 s30, s18
	s_mov_b32 s30, s12
	s_cbranch_scc0 .LBB0_735
	s_branch .LBB0_730

.LBB0_817:
	s_add_i32 s79, s56, 2
	s_add_u32 s58, s54, 0x80
	s_addc_u32 s57, s55, 0
	s_cmp_eq_u32 s74, s56
	s_cselect_b32 s57, s41, s57
	s_cselect_b32 s56, s40, s58
	s_cselect_b32 s59, s53, s78
	s_cselect_b32 s58, s52, s77
	s_add_i32 s80, 0, 0x10000
	v_add_u32_e32 v0, s80, v184
	s_add_i32 s81, 0, 0x14000
	ds_read_b128 v[18:21], v0
	ds_read_b128 v[22:25], v0 offset:1024
	ds_read_b128 v[26:29], v0 offset:2048
	ds_read_b128 v[30:33], v0 offset:3072
	v_add_u32_e32 v0, s81, v184
	ds_read_b128 v[2:5], v0
	ds_read_b128 v[6:9], v0 offset:1024
	ds_read_b128 v[10:13], v0 offset:2048
	ds_read_b128 v[14:17], v0 offset:3072
	v_lshl_add_u64 v[178:179], s[54:55], 0, v[166:167]
	s_add_i32 m0, s64, 0xc000
	ds_read_b128 v[170:173], v185
	ds_read_b128 v[174:177], v185 offset:1024
	ds_read_b128 v[186:189], v185 offset:2048
	ds_read_b128 v[190:193], v185 offset:3072
	ds_read_b128 v[194:197], v185 offset:4096
	ds_read_b128 v[198:201], v185 offset:5120
	ds_read_b128 v[202:205], v185 offset:6144
	ds_read_b128 v[206:209], v185 offset:7168
	global_load_lds_dwordx4 v[178:179], off
	v_lshl_add_u64 v[178:179], s[54:55], 0, v[168:169]
	s_add_i32 m0, s64, 0xe000
	s_nop 0
	global_load_lds_dwordx4 v[178:179], off
	s_waitcnt vmcnt(8)
	s_waitcnt lgkmcnt(0)
	s_barrier
	s_setprio 1
	s_waitcnt lgkmcnt(0)
	v_mfma_scale_f32_16x16x128_f8f6f4 v[158:161], v[18:25], v[170:177], v[158:161], v182, v182 op_sel_hi:[0,0,0]
	v_mfma_scale_f32_16x16x128_f8f6f4 v[154:157], v[26:33], v[170:177], v[154:157], v182, v182 op_sel_hi:[0,0,0]
	v_mfma_scale_f32_16x16x128_f8f6f4 v[142:145], v[18:25], v[186:193], v[142:145], v182, v182 op_sel_hi:[0,0,0]
	v_mfma_scale_f32_16x16x128_f8f6f4 v[138:141], v[26:33], v[186:193], v[138:141], v182, v182 op_sel_hi:[0,0,0]
	v_mfma_scale_f32_16x16x128_f8f6f4 v[126:129], v[18:25], v[194:201], v[126:129], v182, v182 op_sel_hi:[0,0,0]
	v_mfma_scale_f32_16x16x128_f8f6f4 v[122:125], v[26:33], v[194:201], v[122:125], v182, v182 op_sel_hi:[0,0,0]
	v_mfma_scale_f32_16x16x128_f8f6f4 v[110:113], v[18:25], v[202:209], v[110:113], v182, v182 op_sel_hi:[0,0,0]
	v_mfma_scale_f32_16x16x128_f8f6f4 v[106:109], v[26:33], v[202:209], v[106:109], v182, v182 op_sel_hi:[0,0,0]
	v_mfma_scale_f32_16x16x128_f8f6f4 v[150:153], v[2:9], v[170:177], v[150:153], v182, v182 op_sel_hi:[0,0,0]
	v_mfma_scale_f32_16x16x128_f8f6f4 v[146:149], v[10:17], v[170:177], v[146:149], v182, v182 op_sel_hi:[0,0,0]
	v_mfma_scale_f32_16x16x128_f8f6f4 v[134:137], v[2:9], v[186:193], v[134:137], v182, v182 op_sel_hi:[0,0,0]
	v_mfma_scale_f32_16x16x128_f8f6f4 v[130:133], v[10:17], v[186:193], v[130:133], v182, v182 op_sel_hi:[0,0,0]
	v_mfma_scale_f32_16x16x128_f8f6f4 v[118:121], v[2:9], v[194:201], v[118:121], v182, v182 op_sel_hi:[0,0,0]
	v_mfma_scale_f32_16x16x128_f8f6f4 v[114:117], v[10:17], v[194:201], v[114:117], v182, v182 op_sel_hi:[0,0,0]
	v_mfma_scale_f32_16x16x128_f8f6f4 v[102:105], v[2:9], v[202:209], v[102:105], v182, v182 op_sel_hi:[0,0,0]
	v_mfma_scale_f32_16x16x128_f8f6f4 v[98:101], v[10:17], v[202:209], v[98:101], v182, v182 op_sel_hi:[0,0,0]
	s_setprio 0
	s_barrier
	s_add_i32 s80, s80, s63
	v_lshl_add_u64 v[170:171], s[58:59], 0, v[162:163]
	s_mov_b32 m0, s80
	ds_read_b128 v[186:189], v185 offset:16384
	ds_read_b128 v[190:193], v185 offset:17408
	ds_read_b128 v[194:197], v185 offset:18432
	ds_read_b128 v[198:201], v185 offset:19456
	ds_read_b128 v[202:205], v185 offset:20480
	ds_read_b128 v[206:209], v185 offset:21504
	ds_read_b128 v[212:215], v185 offset:22528
	ds_read_b128 v[216:219], v185 offset:23552
	global_load_lds_dwordx4 v[170:171], off
	s_add_i32 m0, s80, 0x2000
	s_add_u32 s58, s58, s8
	s_addc_u32 s59, s59, s9
	v_lshl_add_u64 v[172:173], v[170:171], 0, s[6:7]
	v_lshl_add_u64 v[174:175], s[58:59], 0, v[162:163]
	s_add_i32 s58, s81, s63
	global_load_lds_dwordx4 v[172:173], off
	s_mov_b32 m0, s58
	v_lshl_add_u64 v[176:177], v[174:175], 0, s[6:7]
	global_load_lds_dwordx4 v[174:175], off
	s_add_i32 m0, s58, 0x2000
	v_lshl_add_u64 v[178:179], s[56:57], 0, v[164:165]
	global_load_lds_dwordx4 v[176:177], off
	s_mov_b32 m0, s64
	v_lshl_add_u64 v[180:181], v[178:179], 0, s[6:7]
	global_load_lds_dwordx4 v[178:179], off
	s_mov_b32 m0, s65
	s_nop 0
	global_load_lds_dwordx4 v[180:181], off
	s_waitcnt vmcnt(8)
	s_waitcnt lgkmcnt(0)
	s_barrier
	s_setprio 1
	s_waitcnt lgkmcnt(0)
	v_mfma_scale_f32_16x16x128_f8f6f4 v[94:97], v[18:25], v[186:193], v[94:97], v182, v182 op_sel_hi:[0,0,0]
	v_mfma_scale_f32_16x16x128_f8f6f4 v[90:93], v[26:33], v[186:193], v[90:93], v182, v182 op_sel_hi:[0,0,0]
	v_mfma_scale_f32_16x16x128_f8f6f4 v[78:81], v[18:25], v[194:201], v[78:81], v182, v182 op_sel_hi:[0,0,0]
	v_mfma_scale_f32_16x16x128_f8f6f4 v[74:77], v[26:33], v[194:201], v[74:77], v182, v182 op_sel_hi:[0,0,0]
	v_mfma_scale_f32_16x16x128_f8f6f4 v[62:65], v[18:25], v[202:209], v[62:65], v182, v182 op_sel_hi:[0,0,0]
	v_mfma_scale_f32_16x16x128_f8f6f4 v[58:61], v[26:33], v[202:209], v[58:61], v182, v182 op_sel_hi:[0,0,0]
	v_mfma_scale_f32_16x16x128_f8f6f4 v[46:49], v[18:25], v[212:219], v[46:49], v182, v182 op_sel_hi:[0,0,0]
	v_mfma_scale_f32_16x16x128_f8f6f4 v[42:45], v[26:33], v[212:219], v[42:45], v182, v182 op_sel_hi:[0,0,0]
	v_mfma_scale_f32_16x16x128_f8f6f4 v[86:89], v[2:9], v[186:193], v[86:89], v182, v182 op_sel_hi:[0,0,0]
	v_mfma_scale_f32_16x16x128_f8f6f4 v[82:85], v[10:17], v[186:193], v[82:85], v182, v182 op_sel_hi:[0,0,0]
	v_mfma_scale_f32_16x16x128_f8f6f4 v[70:73], v[2:9], v[194:201], v[70:73], v182, v182 op_sel_hi:[0,0,0]
	v_mfma_scale_f32_16x16x128_f8f6f4 v[66:69], v[10:17], v[194:201], v[66:69], v182, v182 op_sel_hi:[0,0,0]
	v_mfma_scale_f32_16x16x128_f8f6f4 v[54:57], v[2:9], v[202:209], v[54:57], v182, v182 op_sel_hi:[0,0,0]
	v_mfma_scale_f32_16x16x128_f8f6f4 v[50:53], v[10:17], v[202:209], v[50:53], v182, v182 op_sel_hi:[0,0,0]
	v_mfma_scale_f32_16x16x128_f8f6f4 v[38:41], v[2:9], v[212:219], v[38:41], v182, v182 op_sel_hi:[0,0,0]
	v_mfma_scale_f32_16x16x128_f8f6f4 v[34:37], v[10:17], v[212:219], v[34:37], v182, v182 op_sel_hi:[0,0,0]
	s_setprio 0
	s_barrier
	s_add_i32 s58, 0, 0x18000
	v_add_u32_e32 v0, s58, v184
	s_add_i32 s59, 0, 0x1c000
	ds_read_b128 v[2:5], v0
	ds_read_b128 v[6:9], v0 offset:1024
	ds_read_b128 v[10:13], v0 offset:2048
	ds_read_b128 v[14:17], v0 offset:3072
	v_add_u32_e32 v0, s59, v184
	ds_read_b128 v[18:21], v0
	ds_read_b128 v[22:25], v0 offset:1024
	ds_read_b128 v[26:29], v0 offset:2048
	ds_read_b128 v[30:33], v0 offset:3072
	s_add_u32 s56, s56, s8
	s_addc_u32 s57, s57, s9
	s_mov_b32 m0, s66
	v_lshl_add_u64 v[220:221], s[56:57], 0, v[164:165]
	ds_read_b128 v[186:189], v185 offset:32768
	ds_read_b128 v[190:193], v185 offset:33792
	ds_read_b128 v[194:197], v185 offset:34816
	ds_read_b128 v[198:201], v185 offset:35840
	ds_read_b128 v[202:205], v185 offset:36864
	ds_read_b128 v[206:209], v185 offset:37888
	ds_read_b128 v[212:215], v185 offset:38912
	ds_read_b128 v[216:219], v185 offset:39936
	global_load_lds_dwordx4 v[220:221], off
	v_lshl_add_u64 v[220:221], v[220:221], 0, s[6:7]
	s_mov_b32 m0, s67
	s_nop 0
	global_load_lds_dwordx4 v[220:221], off
	s_waitcnt vmcnt(8)
	s_waitcnt lgkmcnt(0)
	s_barrier
	s_setprio 1
	s_waitcnt lgkmcnt(0)
	v_mfma_scale_f32_16x16x128_f8f6f4 v[158:161], v[2:9], v[186:193], v[158:161], v182, v182 op_sel_hi:[0,0,0]
	v_mfma_scale_f32_16x16x128_f8f6f4 v[154:157], v[10:17], v[186:193], v[154:157], v182, v182 op_sel_hi:[0,0,0]
	v_mfma_scale_f32_16x16x128_f8f6f4 v[142:145], v[2:9], v[194:201], v[142:145], v182, v182 op_sel_hi:[0,0,0]
	v_mfma_scale_f32_16x16x128_f8f6f4 v[138:141], v[10:17], v[194:201], v[138:141], v182, v182 op_sel_hi:[0,0,0]
	v_mfma_scale_f32_16x16x128_f8f6f4 v[126:129], v[2:9], v[202:209], v[126:129], v182, v182 op_sel_hi:[0,0,0]
	v_mfma_scale_f32_16x16x128_f8f6f4 v[122:125], v[10:17], v[202:209], v[122:125], v182, v182 op_sel_hi:[0,0,0]
	v_mfma_scale_f32_16x16x128_f8f6f4 v[110:113], v[2:9], v[212:219], v[110:113], v182, v182 op_sel_hi:[0,0,0]
	v_mfma_scale_f32_16x16x128_f8f6f4 v[106:109], v[10:17], v[212:219], v[106:109], v182, v182 op_sel_hi:[0,0,0]
	v_mfma_scale_f32_16x16x128_f8f6f4 v[150:153], v[18:25], v[186:193], v[150:153], v182, v182 op_sel_hi:[0,0,0]
	v_mfma_scale_f32_16x16x128_f8f6f4 v[146:149], v[26:33], v[186:193], v[146:149], v182, v182 op_sel_hi:[0,0,0]
	v_mfma_scale_f32_16x16x128_f8f6f4 v[134:137], v[18:25], v[194:201], v[134:137], v182, v182 op_sel_hi:[0,0,0]
	v_mfma_scale_f32_16x16x128_f8f6f4 v[130:133], v[26:33], v[194:201], v[130:133], v182, v182 op_sel_hi:[0,0,0]
	v_mfma_scale_f32_16x16x128_f8f6f4 v[118:121], v[18:25], v[202:209], v[118:121], v182, v182 op_sel_hi:[0,0,0]
	v_mfma_scale_f32_16x16x128_f8f6f4 v[114:117], v[26:33], v[202:209], v[114:117], v182, v182 op_sel_hi:[0,0,0]
	v_mfma_scale_f32_16x16x128_f8f6f4 v[102:105], v[18:25], v[212:219], v[102:105], v182, v182 op_sel_hi:[0,0,0]
	v_mfma_scale_f32_16x16x128_f8f6f4 v[98:101], v[26:33], v[212:219], v[98:101], v182, v182 op_sel_hi:[0,0,0]
	s_setprio 0
	s_barrier
	s_add_i32 s56, s58, s63
	v_lshl_add_u64 v[170:171], v[170:171], 0, s[36:37]
	s_mov_b32 m0, s56
	ds_read_b128 v[186:189], v185 offset:49152
	ds_read_b128 v[190:193], v185 offset:50176
	ds_read_b128 v[194:197], v185 offset:51200
	ds_read_b128 v[198:201], v185 offset:52224
	ds_read_b128 v[202:205], v185 offset:53248
	ds_read_b128 v[206:209], v185 offset:54272
	ds_read_b128 v[212:215], v185 offset:55296
	ds_read_b128 v[216:219], v185 offset:56320
	global_load_lds_dwordx4 v[170:171], off
	v_lshl_add_u64 v[170:171], v[172:173], 0, s[36:37]
	s_add_i32 m0, s56, 0x2000
	s_add_i32 s56, s59, s63
	global_load_lds_dwordx4 v[170:171], off
	v_lshl_add_u64 v[170:171], v[174:175], 0, s[36:37]
	s_mov_b32 m0, s56
	s_nop 0
	global_load_lds_dwordx4 v[170:171], off
	v_lshl_add_u64 v[170:171], v[176:177], 0, s[36:37]
	s_add_i32 m0, s56, 0x2000
	s_nop 0
	global_load_lds_dwordx4 v[170:171], off
	v_lshl_add_u64 v[170:171], v[178:179], 0, s[36:37]
	s_mov_b32 m0, s72
	s_nop 0
	global_load_lds_dwordx4 v[170:171], off
	v_lshl_add_u64 v[170:171], v[180:181], 0, s[36:37]
	s_mov_b32 m0, s73
	s_nop 0
	global_load_lds_dwordx4 v[170:171], off
	s_waitcnt vmcnt(8)
	s_waitcnt lgkmcnt(0)
	s_barrier
	s_setprio 1
	s_waitcnt lgkmcnt(0)
	v_mfma_scale_f32_16x16x128_f8f6f4 v[94:97], v[2:9], v[186:193], v[94:97], v182, v182 op_sel_hi:[0,0,0]
	v_mfma_scale_f32_16x16x128_f8f6f4 v[90:93], v[10:17], v[186:193], v[90:93], v182, v182 op_sel_hi:[0,0,0]
	v_mfma_scale_f32_16x16x128_f8f6f4 v[78:81], v[2:9], v[194:201], v[78:81], v182, v182 op_sel_hi:[0,0,0]
	v_mfma_scale_f32_16x16x128_f8f6f4 v[74:77], v[10:17], v[194:201], v[74:77], v182, v182 op_sel_hi:[0,0,0]
	v_mfma_scale_f32_16x16x128_f8f6f4 v[62:65], v[2:9], v[202:209], v[62:65], v182, v182 op_sel_hi:[0,0,0]
	v_mfma_scale_f32_16x16x128_f8f6f4 v[58:61], v[10:17], v[202:209], v[58:61], v182, v182 op_sel_hi:[0,0,0]
	v_mfma_scale_f32_16x16x128_f8f6f4 v[46:49], v[2:9], v[212:219], v[46:49], v182, v182 op_sel_hi:[0,0,0]
	v_mfma_scale_f32_16x16x128_f8f6f4 v[42:45], v[10:17], v[212:219], v[42:45], v182, v182 op_sel_hi:[0,0,0]
	v_mfma_scale_f32_16x16x128_f8f6f4 v[86:89], v[18:25], v[186:193], v[86:89], v182, v182 op_sel_hi:[0,0,0]
	v_mfma_scale_f32_16x16x128_f8f6f4 v[82:85], v[26:33], v[186:193], v[82:85], v182, v182 op_sel_hi:[0,0,0]
	v_mfma_scale_f32_16x16x128_f8f6f4 v[70:73], v[18:25], v[194:201], v[70:73], v182, v182 op_sel_hi:[0,0,0]
	v_mfma_scale_f32_16x16x128_f8f6f4 v[66:69], v[26:33], v[194:201], v[66:69], v182, v182 op_sel_hi:[0,0,0]
	v_mfma_scale_f32_16x16x128_f8f6f4 v[54:57], v[18:25], v[202:209], v[54:57], v182, v182 op_sel_hi:[0,0,0]
	v_mfma_scale_f32_16x16x128_f8f6f4 v[50:53], v[26:33], v[202:209], v[50:53], v182, v182 op_sel_hi:[0,0,0]
	v_mfma_scale_f32_16x16x128_f8f6f4 v[38:41], v[18:25], v[212:219], v[38:41], v182, v182 op_sel_hi:[0,0,0]
	v_mfma_scale_f32_16x16x128_f8f6f4 v[34:37], v[26:33], v[212:219], v[34:37], v182, v182 op_sel_hi:[0,0,0]
	s_setprio 0
	s_barrier
	s_add_u32 s54, s54, 0x100
	s_addc_u32 s55, s55, 0
	s_add_u32 s77, s77, 0x100
	s_addc_u32 s78, s78, 0
	s_cmp_ge_i32 s79, s30
	s_mov_b32 s56, s79
	s_cbranch_scc0 .LBB0_817

.LBB0_1194:
	s_cmp_eq_u32 s78, s83
	s_cselect_b64 vcc, -1, 0
	s_add_i32 s83, s83, 2
	s_and_b64 s[62:63], vcc, exec
	s_cselect_b32 s62, 0, s58
	s_cselect_b32 s63, 0, s59
	s_add_u32 s62, s8, s62
	s_addc_u32 s63, s9, s63
	s_add_u32 s84, s56, s58
	s_addc_u32 s85, s57, s59
	s_and_b64 s[64:65], vcc, exec
	s_cselect_b32 s65, s55, s85
	s_cselect_b32 s64, s54, s84
	s_add_i32 s84, 0, 0x10000
	s_add_i32 s85, 0, 0x14000
	v_add_u32_e32 v2, s84, v179
	v_add_u32_e32 v14, s85, v179
	ds_read_b128 v[26:29], v2
	ds_read_b128 v[30:33], v2 offset:1024
	ds_read_b128 v[18:21], v2 offset:2048
	ds_read_b128 v[22:25], v2 offset:3072
	ds_read_b128 v[2:5], v14
	ds_read_b128 v[6:9], v14 offset:1024
	ds_read_b128 v[10:13], v14 offset:2048
	ds_read_b128 v[14:17], v14 offset:3072
	v_cndmask_b32_e32 v0, v176, v168, vcc
	v_cndmask_b32_e32 v192, v178, v170, vcc
	v_cndmask_b32_e32 v169, v180, v172, vcc
	v_cndmask_b32_e32 v171, v182, v174, vcc
	v_lshl_add_u64 v[194:195], s[60:61], 0, v[180:181]
	s_add_i32 m0, s69, 0xc000
	ds_read_b128 v[184:187], v197
	ds_read_b128 v[188:191], v197 offset:1024
	ds_read_b128 v[198:201], v197 offset:2048
	ds_read_b128 v[202:205], v197 offset:3072
	ds_read_b128 v[212:215], v197 offset:4096
	ds_read_b128 v[216:219], v197 offset:5120
	ds_read_b128 v[240:243], v197 offset:6144
	ds_read_b128 v[244:247], v197 offset:7168
	global_load_lds_dwordx4 v[194:195], off
	v_lshl_add_u64 v[194:195], s[60:61], 0, v[182:183]
	s_add_i32 m0, s69, 0xe000
	s_nop 0
	global_load_lds_dwordx4 v[194:195], off
	s_waitcnt vmcnt(8)
	s_waitcnt lgkmcnt(0)
	s_barrier
	s_setprio 1
	s_waitcnt lgkmcnt(0)
	v_mfma_scale_f32_16x16x128_f8f6f4 v[158:161], v[26:33], v[184:191], v[158:161], v196, v196 op_sel_hi:[0,0,0]
	v_mfma_scale_f32_16x16x128_f8f6f4 v[150:153], v[18:25], v[184:191], v[150:153], v196, v196 op_sel_hi:[0,0,0]
	v_mfma_scale_f32_16x16x128_f8f6f4 v[142:145], v[26:33], v[198:205], v[142:145], v196, v196 op_sel_hi:[0,0,0]
	v_mfma_scale_f32_16x16x128_f8f6f4 v[134:137], v[18:25], v[198:205], v[134:137], v196, v196 op_sel_hi:[0,0,0]
	v_mfma_scale_f32_16x16x128_f8f6f4 v[126:129], v[26:33], v[212:219], v[126:129], v196, v196 op_sel_hi:[0,0,0]
	v_mfma_scale_f32_16x16x128_f8f6f4 v[118:121], v[18:25], v[212:219], v[118:121], v196, v196 op_sel_hi:[0,0,0]
	v_mfma_scale_f32_16x16x128_f8f6f4 v[110:113], v[26:33], v[240:247], v[110:113], v196, v196 op_sel_hi:[0,0,0]
	v_mfma_scale_f32_16x16x128_f8f6f4 v[102:105], v[18:25], v[240:247], v[102:105], v196, v196 op_sel_hi:[0,0,0]
	v_mfma_scale_f32_16x16x128_f8f6f4 v[154:157], v[2:9], v[184:191], v[154:157], v196, v196 op_sel_hi:[0,0,0]
	v_mfma_scale_f32_16x16x128_f8f6f4 v[146:149], v[10:17], v[184:191], v[146:149], v196, v196 op_sel_hi:[0,0,0]
	v_mfma_scale_f32_16x16x128_f8f6f4 v[138:141], v[2:9], v[198:205], v[138:141], v196, v196 op_sel_hi:[0,0,0]
	v_mfma_scale_f32_16x16x128_f8f6f4 v[130:133], v[10:17], v[198:205], v[130:133], v196, v196 op_sel_hi:[0,0,0]
	v_mfma_scale_f32_16x16x128_f8f6f4 v[122:125], v[2:9], v[212:219], v[122:125], v196, v196 op_sel_hi:[0,0,0]
	v_mfma_scale_f32_16x16x128_f8f6f4 v[114:117], v[10:17], v[212:219], v[114:117], v196, v196 op_sel_hi:[0,0,0]
	v_mfma_scale_f32_16x16x128_f8f6f4 v[106:109], v[2:9], v[240:247], v[106:109], v196, v196 op_sel_hi:[0,0,0]
	v_mfma_scale_f32_16x16x128_f8f6f4 v[98:101], v[10:17], v[240:247], v[98:101], v196, v196 op_sel_hi:[0,0,0]
	s_setprio 0
	s_barrier
	s_add_i32 s84, s84, s68
	v_lshl_add_u64 v[184:185], s[64:65], 0, v[164:165]
	s_mov_b32 m0, s84
	ds_read_b128 v[198:201], v197 offset:16384
	ds_read_b128 v[202:205], v197 offset:17408
	ds_read_b128 v[212:215], v197 offset:18432
	ds_read_b128 v[216:219], v197 offset:19456
	ds_read_b128 v[240:243], v197 offset:20480
	ds_read_b128 v[244:247], v197 offset:21504
	ds_read_b128 v[220:223], v197 offset:22528
	ds_read_b128 v[224:227], v197 offset:23552
	global_load_lds_dwordx4 v[184:185], off
	s_add_i32 m0, s84, 0x2000
	s_add_u32 s64, s64, s40
	s_addc_u32 s65, s65, s41
	v_lshl_add_u64 v[186:187], v[184:185], 0, s[10:11]
	v_lshl_add_u64 v[188:189], s[64:65], 0, v[164:165]
	s_add_i32 s64, s85, s68
	global_load_lds_dwordx4 v[186:187], off
	s_mov_b32 m0, s64
	v_lshl_add_u64 v[190:191], v[188:189], 0, s[10:11]
	global_load_lds_dwordx4 v[188:189], off
	s_add_i32 m0, s64, 0x2000
	v_mov_b32_e32 v193, v1
	global_load_lds_dwordx4 v[190:191], off
	s_mov_b32 m0, s69
	v_lshl_add_u64 v[194:195], s[62:63], 0, v[0:1]
	global_load_lds_dwordx4 v0, s[62:63]
	s_mov_b32 m0, s72
	s_nop 0
	global_load_lds_dwordx4 v192, s[62:63]
	s_waitcnt vmcnt(8)
	s_waitcnt lgkmcnt(0)
	v_lshl_add_u64 v[192:193], s[62:63], 0, v[192:193]
	s_barrier
	s_setprio 1
	s_waitcnt lgkmcnt(0)
	v_mfma_scale_f32_16x16x128_f8f6f4 v[94:97], v[26:33], v[198:205], v[94:97], v196, v196 op_sel_hi:[0,0,0]
	v_mfma_scale_f32_16x16x128_f8f6f4 v[86:89], v[18:25], v[198:205], v[86:89], v196, v196 op_sel_hi:[0,0,0]
	v_mfma_scale_f32_16x16x128_f8f6f4 v[78:81], v[26:33], v[212:219], v[78:81], v196, v196 op_sel_hi:[0,0,0]
	v_mfma_scale_f32_16x16x128_f8f6f4 v[70:73], v[18:25], v[212:219], v[70:73], v196, v196 op_sel_hi:[0,0,0]
	v_mfma_scale_f32_16x16x128_f8f6f4 v[62:65], v[26:33], v[240:247], v[62:65], v196, v196 op_sel_hi:[0,0,0]
	v_mfma_scale_f32_16x16x128_f8f6f4 v[54:57], v[18:25], v[240:247], v[54:57], v196, v196 op_sel_hi:[0,0,0]
	v_mfma_scale_f32_16x16x128_f8f6f4 v[46:49], v[26:33], v[220:227], v[46:49], v196, v196 op_sel_hi:[0,0,0]
	v_mfma_scale_f32_16x16x128_f8f6f4 v[38:41], v[18:25], v[220:227], v[38:41], v196, v196 op_sel_hi:[0,0,0]
	v_mfma_scale_f32_16x16x128_f8f6f4 v[90:93], v[2:9], v[198:205], v[90:93], v196, v196 op_sel_hi:[0,0,0]
	v_mfma_scale_f32_16x16x128_f8f6f4 v[82:85], v[10:17], v[198:205], v[82:85], v196, v196 op_sel_hi:[0,0,0]
	v_mfma_scale_f32_16x16x128_f8f6f4 v[74:77], v[2:9], v[212:219], v[74:77], v196, v196 op_sel_hi:[0,0,0]
	v_mfma_scale_f32_16x16x128_f8f6f4 v[66:69], v[10:17], v[212:219], v[66:69], v196, v196 op_sel_hi:[0,0,0]
	v_mfma_scale_f32_16x16x128_f8f6f4 v[58:61], v[2:9], v[240:247], v[58:61], v196, v196 op_sel_hi:[0,0,0]
	v_mfma_scale_f32_16x16x128_f8f6f4 v[50:53], v[10:17], v[240:247], v[50:53], v196, v196 op_sel_hi:[0,0,0]
	v_mfma_scale_f32_16x16x128_f8f6f4 v[42:45], v[2:9], v[220:227], v[42:45], v196, v196 op_sel_hi:[0,0,0]
	v_mfma_scale_f32_16x16x128_f8f6f4 v[34:37], v[10:17], v[220:227], v[34:37], v196, v196 op_sel_hi:[0,0,0]
	s_setprio 0
	s_barrier
	s_add_i32 s64, 0, 0x18000
	v_add_u32_e32 v0, s64, v179
	s_add_i32 s65, 0, 0x1c000
	ds_read_b128 v[2:5], v0
	ds_read_b128 v[6:9], v0 offset:1024
	ds_read_b128 v[10:13], v0 offset:2048
	ds_read_b128 v[14:17], v0 offset:3072
	v_add_u32_e32 v0, s65, v179
	ds_read_b128 v[18:21], v0
	ds_read_b128 v[22:25], v0 offset:1024
	ds_read_b128 v[26:29], v0 offset:2048
	ds_read_b128 v[30:33], v0 offset:3072
	s_mov_b32 m0, s73
	ds_read_b128 v[198:201], v197 offset:32768
	ds_read_b128 v[202:205], v197 offset:33792
	ds_read_b128 v[212:215], v197 offset:34816
	ds_read_b128 v[216:219], v197 offset:35840
	ds_read_b128 v[220:223], v197 offset:36864
	ds_read_b128 v[224:227], v197 offset:37888
	ds_read_b128 v[240:243], v197 offset:38912
	ds_read_b128 v[244:247], v197 offset:39936
	global_load_lds_dwordx4 v169, s[62:63]
	s_mov_b32 m0, s74
	s_nop 0
	global_load_lds_dwordx4 v171, s[62:63]
	s_waitcnt vmcnt(8)
	s_waitcnt lgkmcnt(0)
	s_barrier
	s_setprio 1
	s_waitcnt lgkmcnt(0)
	v_mfma_scale_f32_16x16x128_f8f6f4 v[158:161], v[2:9], v[198:205], v[158:161], v196, v196 op_sel_hi:[0,0,0]
	v_mfma_scale_f32_16x16x128_f8f6f4 v[150:153], v[10:17], v[198:205], v[150:153], v196, v196 op_sel_hi:[0,0,0]
	v_mfma_scale_f32_16x16x128_f8f6f4 v[142:145], v[2:9], v[212:219], v[142:145], v196, v196 op_sel_hi:[0,0,0]
	v_mfma_scale_f32_16x16x128_f8f6f4 v[134:137], v[10:17], v[212:219], v[134:137], v196, v196 op_sel_hi:[0,0,0]
	v_mfma_scale_f32_16x16x128_f8f6f4 v[126:129], v[2:9], v[220:227], v[126:129], v196, v196 op_sel_hi:[0,0,0]
	v_mfma_scale_f32_16x16x128_f8f6f4 v[118:121], v[10:17], v[220:227], v[118:121], v196, v196 op_sel_hi:[0,0,0]
	v_mfma_scale_f32_16x16x128_f8f6f4 v[110:113], v[2:9], v[240:247], v[110:113], v196, v196 op_sel_hi:[0,0,0]
	v_mfma_scale_f32_16x16x128_f8f6f4 v[102:105], v[10:17], v[240:247], v[102:105], v196, v196 op_sel_hi:[0,0,0]
	v_mfma_scale_f32_16x16x128_f8f6f4 v[154:157], v[18:25], v[198:205], v[154:157], v196, v196 op_sel_hi:[0,0,0]
	v_mfma_scale_f32_16x16x128_f8f6f4 v[146:149], v[26:33], v[198:205], v[146:149], v196, v196 op_sel_hi:[0,0,0]
	v_mfma_scale_f32_16x16x128_f8f6f4 v[138:141], v[18:25], v[212:219], v[138:141], v196, v196 op_sel_hi:[0,0,0]
	v_mfma_scale_f32_16x16x128_f8f6f4 v[130:133], v[26:33], v[212:219], v[130:133], v196, v196 op_sel_hi:[0,0,0]
	v_mfma_scale_f32_16x16x128_f8f6f4 v[122:125], v[18:25], v[220:227], v[122:125], v196, v196 op_sel_hi:[0,0,0]
	v_mfma_scale_f32_16x16x128_f8f6f4 v[114:117], v[26:33], v[220:227], v[114:117], v196, v196 op_sel_hi:[0,0,0]
	v_mfma_scale_f32_16x16x128_f8f6f4 v[106:109], v[18:25], v[240:247], v[106:109], v196, v196 op_sel_hi:[0,0,0]
	v_mfma_scale_f32_16x16x128_f8f6f4 v[98:101], v[26:33], v[240:247], v[98:101], v196, v196 op_sel_hi:[0,0,0]
	s_setprio 0
	s_barrier
	s_add_i32 s62, s64, s68
	v_lshl_add_u64 v[184:185], v[184:185], 0, s[36:37]
	s_mov_b32 m0, s62
	ds_read_b128 v[198:201], v197 offset:49152
	ds_read_b128 v[202:205], v197 offset:50176
	ds_read_b128 v[212:215], v197 offset:51200
	ds_read_b128 v[216:219], v197 offset:52224
	ds_read_b128 v[220:223], v197 offset:53248
	ds_read_b128 v[224:227], v197 offset:54272
	ds_read_b128 v[240:243], v197 offset:55296
	ds_read_b128 v[244:247], v197 offset:56320
	global_load_lds_dwordx4 v[184:185], off
	v_lshl_add_u64 v[184:185], v[186:187], 0, s[36:37]
	s_add_i32 m0, s62, 0x2000
	s_add_i32 s62, s65, s68
	global_load_lds_dwordx4 v[184:185], off
	v_lshl_add_u64 v[184:185], v[188:189], 0, s[36:37]
	s_mov_b32 m0, s62
	s_nop 0
	global_load_lds_dwordx4 v[184:185], off
	v_lshl_add_u64 v[184:185], v[190:191], 0, s[36:37]
	s_add_i32 m0, s62, 0x2000
	s_nop 0
	global_load_lds_dwordx4 v[184:185], off
	v_lshl_add_u64 v[184:185], v[194:195], 0, s[36:37]
	s_mov_b32 m0, s76
	s_nop 0
	global_load_lds_dwordx4 v[184:185], off
	v_lshl_add_u64 v[184:185], v[192:193], 0, s[36:37]
	s_mov_b32 m0, s77
	s_nop 0
	global_load_lds_dwordx4 v[184:185], off
	s_waitcnt vmcnt(8)
	s_waitcnt lgkmcnt(0)
	s_barrier
	s_setprio 1
	s_waitcnt lgkmcnt(0)
	v_mfma_scale_f32_16x16x128_f8f6f4 v[94:97], v[2:9], v[198:205], v[94:97], v196, v196 op_sel_hi:[0,0,0]
	v_mfma_scale_f32_16x16x128_f8f6f4 v[86:89], v[10:17], v[198:205], v[86:89], v196, v196 op_sel_hi:[0,0,0]
	v_mfma_scale_f32_16x16x128_f8f6f4 v[78:81], v[2:9], v[212:219], v[78:81], v196, v196 op_sel_hi:[0,0,0]
	v_mfma_scale_f32_16x16x128_f8f6f4 v[70:73], v[10:17], v[212:219], v[70:73], v196, v196 op_sel_hi:[0,0,0]
	v_mfma_scale_f32_16x16x128_f8f6f4 v[62:65], v[2:9], v[220:227], v[62:65], v196, v196 op_sel_hi:[0,0,0]
	v_mfma_scale_f32_16x16x128_f8f6f4 v[54:57], v[10:17], v[220:227], v[54:57], v196, v196 op_sel_hi:[0,0,0]
	v_mfma_scale_f32_16x16x128_f8f6f4 v[46:49], v[2:9], v[240:247], v[46:49], v196, v196 op_sel_hi:[0,0,0]
	v_mfma_scale_f32_16x16x128_f8f6f4 v[38:41], v[10:17], v[240:247], v[38:41], v196, v196 op_sel_hi:[0,0,0]
	v_mfma_scale_f32_16x16x128_f8f6f4 v[90:93], v[18:25], v[198:205], v[90:93], v196, v196 op_sel_hi:[0,0,0]
	v_mfma_scale_f32_16x16x128_f8f6f4 v[82:85], v[26:33], v[198:205], v[82:85], v196, v196 op_sel_hi:[0,0,0]
	v_mfma_scale_f32_16x16x128_f8f6f4 v[74:77], v[18:25], v[212:219], v[74:77], v196, v196 op_sel_hi:[0,0,0]
	v_mfma_scale_f32_16x16x128_f8f6f4 v[66:69], v[26:33], v[212:219], v[66:69], v196, v196 op_sel_hi:[0,0,0]
	v_mfma_scale_f32_16x16x128_f8f6f4 v[58:61], v[18:25], v[220:227], v[58:61], v196, v196 op_sel_hi:[0,0,0]
	v_mfma_scale_f32_16x16x128_f8f6f4 v[50:53], v[26:33], v[220:227], v[50:53], v196, v196 op_sel_hi:[0,0,0]
	v_mfma_scale_f32_16x16x128_f8f6f4 v[42:45], v[18:25], v[240:247], v[42:45], v196, v196 op_sel_hi:[0,0,0]
	v_mfma_scale_f32_16x16x128_f8f6f4 v[34:37], v[26:33], v[240:247], v[34:37], v196, v196 op_sel_hi:[0,0,0]
	s_setprio 0
	s_barrier
	s_add_u32 s58, s58, 0x100
	s_addc_u32 s59, s59, 0
	s_add_u32 s60, s60, 0x100
	s_addc_u32 s61, s61, 0
	s_cmp_ge_i32 s83, s7
	s_cbranch_scc0 .LBB0_1194

.LBB0_1289:
	s_add_i32 s82, s56, 2
	s_add_u32 s58, s54, 0x80
	s_addc_u32 s57, s55, 0
	s_cmp_eq_u32 s72, s56
	s_cselect_b32 s57, s51, s57
	s_cselect_b32 s56, s50, s58
	s_cselect_b32 s59, s53, s81
	s_cselect_b32 s58, s52, s80
	s_add_i32 s83, 0, 0x10000
	s_add_i32 s84, 0, 0x14000
	v_add_u32_e32 v2, s83, v182
	v_add_u32_e32 v14, s84, v182
	ds_read_b128 v[18:21], v2
	ds_read_b128 v[22:25], v2 offset:1024
	ds_read_b128 v[26:29], v2 offset:2048
	ds_read_b128 v[30:33], v2 offset:3072
	ds_read_b128 v[2:5], v14
	ds_read_b128 v[6:9], v14 offset:1024
	ds_read_b128 v[10:13], v14 offset:2048
	ds_read_b128 v[14:17], v14 offset:3072
	v_lshl_add_u64 v[176:177], s[54:55], 0, v[164:165]
	s_add_i32 m0, s65, 0xc000
	ds_read_b128 v[168:171], v183
	ds_read_b128 v[172:175], v183 offset:1024
	ds_read_b128 v[184:187], v183 offset:2048
	ds_read_b128 v[188:191], v183 offset:3072
	ds_read_b128 v[192:195], v183 offset:4096
	ds_read_b128 v[196:199], v183 offset:5120
	ds_read_b128 v[200:203], v183 offset:6144
	ds_read_b128 v[204:207], v183 offset:7168
	global_load_lds_dwordx4 v[176:177], off
	v_lshl_add_u64 v[176:177], s[54:55], 0, v[166:167]
	s_add_i32 m0, s65, 0xe000
	s_nop 0
	global_load_lds_dwordx4 v[176:177], off
	s_waitcnt vmcnt(8)
	s_waitcnt lgkmcnt(0)
	s_barrier
	s_setprio 1
	s_waitcnt lgkmcnt(0)
	v_mfma_scale_f32_16x16x128_f8f6f4 v[158:161], v[18:25], v[168:175], v[158:161], v180, v180 op_sel_hi:[0,0,0]
	v_mfma_scale_f32_16x16x128_f8f6f4 v[154:157], v[26:33], v[168:175], v[154:157], v180, v180 op_sel_hi:[0,0,0]
	v_mfma_scale_f32_16x16x128_f8f6f4 v[150:153], v[18:25], v[184:191], v[150:153], v180, v180 op_sel_hi:[0,0,0]
	v_mfma_scale_f32_16x16x128_f8f6f4 v[146:149], v[26:33], v[184:191], v[146:149], v180, v180 op_sel_hi:[0,0,0]
	v_mfma_scale_f32_16x16x128_f8f6f4 v[138:141], v[18:25], v[192:199], v[138:141], v180, v180 op_sel_hi:[0,0,0]
	v_mfma_scale_f32_16x16x128_f8f6f4 v[130:133], v[26:33], v[192:199], v[130:133], v180, v180 op_sel_hi:[0,0,0]
	v_mfma_scale_f32_16x16x128_f8f6f4 v[122:125], v[18:25], v[200:207], v[122:125], v180, v180 op_sel_hi:[0,0,0]
	v_mfma_scale_f32_16x16x128_f8f6f4 v[114:117], v[26:33], v[200:207], v[114:117], v180, v180 op_sel_hi:[0,0,0]
	v_mfma_scale_f32_16x16x128_f8f6f4 v[142:145], v[2:9], v[168:175], v[142:145], v180, v180 op_sel_hi:[0,0,0]
	v_mfma_scale_f32_16x16x128_f8f6f4 v[134:137], v[10:17], v[168:175], v[134:137], v180, v180 op_sel_hi:[0,0,0]
	v_mfma_scale_f32_16x16x128_f8f6f4 v[126:129], v[2:9], v[184:191], v[126:129], v180, v180 op_sel_hi:[0,0,0]
	v_mfma_scale_f32_16x16x128_f8f6f4 v[118:121], v[10:17], v[184:191], v[118:121], v180, v180 op_sel_hi:[0,0,0]
	v_mfma_scale_f32_16x16x128_f8f6f4 v[110:113], v[2:9], v[192:199], v[110:113], v180, v180 op_sel_hi:[0,0,0]
	v_mfma_scale_f32_16x16x128_f8f6f4 v[106:109], v[10:17], v[192:199], v[106:109], v180, v180 op_sel_hi:[0,0,0]
	v_mfma_scale_f32_16x16x128_f8f6f4 v[102:105], v[2:9], v[200:207], v[102:105], v180, v180 op_sel_hi:[0,0,0]
	v_mfma_scale_f32_16x16x128_f8f6f4 v[98:101], v[10:17], v[200:207], v[98:101], v180, v180 op_sel_hi:[0,0,0]
	s_setprio 0
	s_barrier
	s_add_i32 s83, s83, s64
	v_lshl_add_u64 v[168:169], s[58:59], 0, v[0:1]
	s_mov_b32 m0, s83
	ds_read_b128 v[184:187], v183 offset:16384
	ds_read_b128 v[188:191], v183 offset:17408
	ds_read_b128 v[192:195], v183 offset:18432
	ds_read_b128 v[196:199], v183 offset:19456
	ds_read_b128 v[200:203], v183 offset:20480
	ds_read_b128 v[204:207], v183 offset:21504
	ds_read_b128 v[212:215], v183 offset:22528
	ds_read_b128 v[216:219], v183 offset:23552
	global_load_lds_dwordx4 v[168:169], off
	s_add_i32 m0, s83, 0x2000
	s_add_u32 s58, s58, s8
	s_addc_u32 s59, s59, s9
	v_lshl_add_u64 v[170:171], v[168:169], 0, s[6:7]
	v_lshl_add_u64 v[172:173], s[58:59], 0, v[0:1]
	s_add_i32 s58, s84, s64
	global_load_lds_dwordx4 v[170:171], off
	s_mov_b32 m0, s58
	v_lshl_add_u64 v[174:175], v[172:173], 0, s[6:7]
	global_load_lds_dwordx4 v[172:173], off
	s_add_i32 m0, s58, 0x2000
	v_lshl_add_u64 v[176:177], s[56:57], 0, v[162:163]
	global_load_lds_dwordx4 v[174:175], off
	s_mov_b32 m0, s65
	v_lshl_add_u64 v[178:179], v[176:177], 0, s[10:11]
	global_load_lds_dwordx4 v[176:177], off
	s_mov_b32 m0, s66
	s_nop 0
	global_load_lds_dwordx4 v[178:179], off
	s_waitcnt vmcnt(8)
	s_waitcnt lgkmcnt(0)
	s_barrier
	s_setprio 1
	s_waitcnt lgkmcnt(0)
	v_mfma_scale_f32_16x16x128_f8f6f4 v[94:97], v[18:25], v[184:191], v[94:97], v180, v180 op_sel_hi:[0,0,0]
	v_mfma_scale_f32_16x16x128_f8f6f4 v[90:93], v[26:33], v[184:191], v[90:93], v180, v180 op_sel_hi:[0,0,0]
	v_mfma_scale_f32_16x16x128_f8f6f4 v[86:89], v[18:25], v[192:199], v[86:89], v180, v180 op_sel_hi:[0,0,0]
	v_mfma_scale_f32_16x16x128_f8f6f4 v[82:85], v[26:33], v[192:199], v[82:85], v180, v180 op_sel_hi:[0,0,0]
	v_mfma_scale_f32_16x16x128_f8f6f4 v[74:77], v[18:25], v[200:207], v[74:77], v180, v180 op_sel_hi:[0,0,0]
	v_mfma_scale_f32_16x16x128_f8f6f4 v[66:69], v[26:33], v[200:207], v[66:69], v180, v180 op_sel_hi:[0,0,0]
	v_mfma_scale_f32_16x16x128_f8f6f4 v[58:61], v[18:25], v[212:219], v[58:61], v180, v180 op_sel_hi:[0,0,0]
	v_mfma_scale_f32_16x16x128_f8f6f4 v[50:53], v[26:33], v[212:219], v[50:53], v180, v180 op_sel_hi:[0,0,0]
	v_mfma_scale_f32_16x16x128_f8f6f4 v[78:81], v[2:9], v[184:191], v[78:81], v180, v180 op_sel_hi:[0,0,0]
	v_mfma_scale_f32_16x16x128_f8f6f4 v[70:73], v[10:17], v[184:191], v[70:73], v180, v180 op_sel_hi:[0,0,0]
	v_mfma_scale_f32_16x16x128_f8f6f4 v[62:65], v[2:9], v[192:199], v[62:65], v180, v180 op_sel_hi:[0,0,0]
	v_mfma_scale_f32_16x16x128_f8f6f4 v[54:57], v[10:17], v[192:199], v[54:57], v180, v180 op_sel_hi:[0,0,0]
	v_mfma_scale_f32_16x16x128_f8f6f4 v[46:49], v[2:9], v[200:207], v[46:49], v180, v180 op_sel_hi:[0,0,0]
	v_mfma_scale_f32_16x16x128_f8f6f4 v[42:45], v[10:17], v[200:207], v[42:45], v180, v180 op_sel_hi:[0,0,0]
	v_mfma_scale_f32_16x16x128_f8f6f4 v[38:41], v[2:9], v[212:219], v[38:41], v180, v180 op_sel_hi:[0,0,0]
	v_mfma_scale_f32_16x16x128_f8f6f4 v[34:37], v[10:17], v[212:219], v[34:37], v180, v180 op_sel_hi:[0,0,0]
	s_setprio 0
	s_barrier
	s_add_i32 s58, 0, 0x18000
	s_add_i32 s59, 0, 0x1c000
	v_add_u32_e32 v14, s58, v182
	v_add_u32_e32 v30, s59, v182
	ds_read_b128 v[2:5], v14
	ds_read_b128 v[6:9], v14 offset:1024
	ds_read_b128 v[10:13], v14 offset:2048
	ds_read_b128 v[14:17], v14 offset:3072
	ds_read_b128 v[18:21], v30
	ds_read_b128 v[22:25], v30 offset:1024
	ds_read_b128 v[26:29], v30 offset:2048
	ds_read_b128 v[30:33], v30 offset:3072
	s_add_u32 s56, s56, s6
	s_addc_u32 s57, s57, s7
	s_mov_b32 m0, s67
	v_lshl_add_u64 v[208:209], s[56:57], 0, v[162:163]
	ds_read_b128 v[184:187], v183 offset:32768
	ds_read_b128 v[188:191], v183 offset:33792
	ds_read_b128 v[192:195], v183 offset:34816
	ds_read_b128 v[196:199], v183 offset:35840
	ds_read_b128 v[200:203], v183 offset:36864
	ds_read_b128 v[204:207], v183 offset:37888
	ds_read_b128 v[212:215], v183 offset:38912
	ds_read_b128 v[216:219], v183 offset:39936
	global_load_lds_dwordx4 v[208:209], off
	v_lshl_add_u64 v[208:209], v[208:209], 0, s[10:11]
	s_mov_b32 m0, s68
	s_nop 0
	global_load_lds_dwordx4 v[208:209], off
	s_waitcnt vmcnt(8)
	s_waitcnt lgkmcnt(0)
	s_barrier
	s_setprio 1
	s_waitcnt lgkmcnt(0)
	v_mfma_scale_f32_16x16x128_f8f6f4 v[158:161], v[2:9], v[184:191], v[158:161], v180, v180 op_sel_hi:[0,0,0]
	v_mfma_scale_f32_16x16x128_f8f6f4 v[154:157], v[10:17], v[184:191], v[154:157], v180, v180 op_sel_hi:[0,0,0]
	v_mfma_scale_f32_16x16x128_f8f6f4 v[150:153], v[2:9], v[192:199], v[150:153], v180, v180 op_sel_hi:[0,0,0]
	v_mfma_scale_f32_16x16x128_f8f6f4 v[146:149], v[10:17], v[192:199], v[146:149], v180, v180 op_sel_hi:[0,0,0]
	v_mfma_scale_f32_16x16x128_f8f6f4 v[138:141], v[2:9], v[200:207], v[138:141], v180, v180 op_sel_hi:[0,0,0]
	v_mfma_scale_f32_16x16x128_f8f6f4 v[130:133], v[10:17], v[200:207], v[130:133], v180, v180 op_sel_hi:[0,0,0]
	v_mfma_scale_f32_16x16x128_f8f6f4 v[122:125], v[2:9], v[212:219], v[122:125], v180, v180 op_sel_hi:[0,0,0]
	v_mfma_scale_f32_16x16x128_f8f6f4 v[114:117], v[10:17], v[212:219], v[114:117], v180, v180 op_sel_hi:[0,0,0]
	v_mfma_scale_f32_16x16x128_f8f6f4 v[142:145], v[18:25], v[184:191], v[142:145], v180, v180 op_sel_hi:[0,0,0]
	v_mfma_scale_f32_16x16x128_f8f6f4 v[134:137], v[26:33], v[184:191], v[134:137], v180, v180 op_sel_hi:[0,0,0]
	v_mfma_scale_f32_16x16x128_f8f6f4 v[126:129], v[18:25], v[192:199], v[126:129], v180, v180 op_sel_hi:[0,0,0]
	v_mfma_scale_f32_16x16x128_f8f6f4 v[118:121], v[26:33], v[192:199], v[118:121], v180, v180 op_sel_hi:[0,0,0]
	v_mfma_scale_f32_16x16x128_f8f6f4 v[110:113], v[18:25], v[200:207], v[110:113], v180, v180 op_sel_hi:[0,0,0]
	v_mfma_scale_f32_16x16x128_f8f6f4 v[106:109], v[26:33], v[200:207], v[106:109], v180, v180 op_sel_hi:[0,0,0]
	v_mfma_scale_f32_16x16x128_f8f6f4 v[102:105], v[18:25], v[212:219], v[102:105], v180, v180 op_sel_hi:[0,0,0]
	v_mfma_scale_f32_16x16x128_f8f6f4 v[98:101], v[26:33], v[212:219], v[98:101], v180, v180 op_sel_hi:[0,0,0]
	s_setprio 0
	s_barrier
	s_add_i32 s56, s58, s64
	v_lshl_add_u64 v[168:169], v[168:169], 0, s[36:37]
	s_mov_b32 m0, s56
	ds_read_b128 v[184:187], v183 offset:49152
	ds_read_b128 v[188:191], v183 offset:50176
	ds_read_b128 v[192:195], v183 offset:51200
	ds_read_b128 v[196:199], v183 offset:52224
	ds_read_b128 v[200:203], v183 offset:53248
	ds_read_b128 v[204:207], v183 offset:54272
	ds_read_b128 v[212:215], v183 offset:55296
	ds_read_b128 v[216:219], v183 offset:56320
	global_load_lds_dwordx4 v[168:169], off
	v_lshl_add_u64 v[168:169], v[170:171], 0, s[36:37]
	s_add_i32 m0, s56, 0x2000
	s_add_i32 s56, s59, s64
	global_load_lds_dwordx4 v[168:169], off
	v_lshl_add_u64 v[168:169], v[172:173], 0, s[36:37]
	s_mov_b32 m0, s56
	s_nop 0
	global_load_lds_dwordx4 v[168:169], off
	v_lshl_add_u64 v[168:169], v[174:175], 0, s[36:37]
	s_add_i32 m0, s56, 0x2000
	s_nop 0
	global_load_lds_dwordx4 v[168:169], off
	v_lshl_add_u64 v[168:169], v[176:177], 0, s[36:37]
	s_mov_b32 m0, s12
	s_nop 0
	global_load_lds_dwordx4 v[168:169], off
	v_lshl_add_u64 v[168:169], v[178:179], 0, s[36:37]
	s_mov_b32 m0, s70
	s_nop 0
	global_load_lds_dwordx4 v[168:169], off
	s_waitcnt vmcnt(8)
	s_waitcnt lgkmcnt(0)
	s_barrier
	s_setprio 1
	s_waitcnt lgkmcnt(0)
	v_mfma_scale_f32_16x16x128_f8f6f4 v[94:97], v[2:9], v[184:191], v[94:97], v180, v180 op_sel_hi:[0,0,0]
	v_mfma_scale_f32_16x16x128_f8f6f4 v[90:93], v[10:17], v[184:191], v[90:93], v180, v180 op_sel_hi:[0,0,0]
	v_mfma_scale_f32_16x16x128_f8f6f4 v[86:89], v[2:9], v[192:199], v[86:89], v180, v180 op_sel_hi:[0,0,0]
	v_mfma_scale_f32_16x16x128_f8f6f4 v[82:85], v[10:17], v[192:199], v[82:85], v180, v180 op_sel_hi:[0,0,0]
	v_mfma_scale_f32_16x16x128_f8f6f4 v[74:77], v[2:9], v[200:207], v[74:77], v180, v180 op_sel_hi:[0,0,0]
	v_mfma_scale_f32_16x16x128_f8f6f4 v[66:69], v[10:17], v[200:207], v[66:69], v180, v180 op_sel_hi:[0,0,0]
	v_mfma_scale_f32_16x16x128_f8f6f4 v[58:61], v[2:9], v[212:219], v[58:61], v180, v180 op_sel_hi:[0,0,0]
	v_mfma_scale_f32_16x16x128_f8f6f4 v[50:53], v[10:17], v[212:219], v[50:53], v180, v180 op_sel_hi:[0,0,0]
	v_mfma_scale_f32_16x16x128_f8f6f4 v[78:81], v[18:25], v[184:191], v[78:81], v180, v180 op_sel_hi:[0,0,0]
	v_mfma_scale_f32_16x16x128_f8f6f4 v[70:73], v[26:33], v[184:191], v[70:73], v180, v180 op_sel_hi:[0,0,0]
	v_mfma_scale_f32_16x16x128_f8f6f4 v[62:65], v[18:25], v[192:199], v[62:65], v180, v180 op_sel_hi:[0,0,0]
	v_mfma_scale_f32_16x16x128_f8f6f4 v[54:57], v[26:33], v[192:199], v[54:57], v180, v180 op_sel_hi:[0,0,0]
	v_mfma_scale_f32_16x16x128_f8f6f4 v[46:49], v[18:25], v[200:207], v[46:49], v180, v180 op_sel_hi:[0,0,0]
	v_mfma_scale_f32_16x16x128_f8f6f4 v[42:45], v[26:33], v[200:207], v[42:45], v180, v180 op_sel_hi:[0,0,0]
	v_mfma_scale_f32_16x16x128_f8f6f4 v[38:41], v[18:25], v[212:219], v[38:41], v180, v180 op_sel_hi:[0,0,0]
	v_mfma_scale_f32_16x16x128_f8f6f4 v[34:37], v[26:33], v[212:219], v[34:37], v180, v180 op_sel_hi:[0,0,0]
	s_setprio 0
	s_barrier
	s_add_u32 s54, s54, 0x100
	s_addc_u32 s55, s55, 0
	s_add_u32 s80, s80, 0x100
	s_addc_u32 s81, s81, 0
	s_cmp_ge_i32 s82, s18
	s_mov_b32 s56, s82
	s_cbranch_scc0 .LBB0_1289
	v_pk_mul_f32 v[160:161], v[160:161], s[2:3] op_sel_hi:[1,0]
	v_pk_mul_f32 v[158:159], v[158:159], s[2:3] op_sel_hi:[1,0]
	v_pk_mul_f32 v[156:157], v[156:157], s[2:3] op_sel_hi:[1,0]
	v_pk_mul_f32 v[154:155], v[154:155], s[2:3] op_sel_hi:[1,0]
	v_pk_mul_f32 v[170:171], v[144:145], s[2:3] op_sel_hi:[1,0]
	v_pk_mul_f32 v[172:173], v[142:143], s[2:3] op_sel_hi:[1,0]
	v_pk_mul_f32 v[168:169], v[136:137], s[2:3] op_sel_hi:[1,0]
	v_pk_mul_f32 v[174:175], v[134:135], s[2:3] op_sel_hi:[1,0]
	v_pk_mul_f32 v[136:137], v[152:153], s[2:3] op_sel_hi:[1,0]
	v_pk_mul_f32 v[142:143], v[150:151], s[2:3] op_sel_hi:[1,0]
	v_pk_mul_f32 v[134:135], v[148:149], s[2:3] op_sel_hi:[1,0]
	v_pk_mul_f32 v[144:145], v[146:147], s[2:3] op_sel_hi:[1,0]
	v_pk_mul_f32 v[148:149], v[128:129], s[2:3] op_sel_hi:[1,0]
	v_pk_mul_f32 v[150:151], v[126:127], s[2:3] op_sel_hi:[1,0]
	v_pk_mul_f32 v[146:147], v[120:121], s[2:3] op_sel_hi:[1,0]
	v_pk_mul_f32 v[152:153], v[118:119], s[2:3] op_sel_hi:[1,0]
	v_pk_mul_f32 v[120:121], v[140:141], s[2:3] op_sel_hi:[1,0]
	v_pk_mul_f32 v[126:127], v[138:139], s[2:3] op_sel_hi:[1,0]
	v_pk_mul_f32 v[118:119], v[132:133], s[2:3] op_sel_hi:[1,0]
	v_pk_mul_f32 v[128:129], v[130:131], s[2:3] op_sel_hi:[1,0]
	v_pk_mul_f32 v[132:133], v[112:113], s[2:3] op_sel_hi:[1,0]
	v_pk_mul_f32 v[138:139], v[110:111], s[2:3] op_sel_hi:[1,0]
	v_pk_mul_f32 v[130:131], v[108:109], s[2:3] op_sel_hi:[1,0]
	v_pk_mul_f32 v[140:141], v[106:107], s[2:3] op_sel_hi:[1,0]
	v_pk_mul_f32 v[108:109], v[124:125], s[2:3] op_sel_hi:[1,0]
	v_pk_mul_f32 v[110:111], v[122:123], s[2:3] op_sel_hi:[1,0]
	v_pk_mul_f32 v[106:107], v[116:117], s[2:3] op_sel_hi:[1,0]
	v_pk_mul_f32 v[112:113], v[114:115], s[2:3] op_sel_hi:[1,0]
	v_pk_mul_f32 v[104:105], v[104:105], s[2:3] op_sel_hi:[1,0]
	v_pk_mul_f32 v[102:103], v[102:103], s[2:3] op_sel_hi:[1,0]
	v_pk_mul_f32 v[100:101], v[100:101], s[2:3] op_sel_hi:[1,0]
	v_pk_mul_f32 v[98:99], v[98:99], s[2:3] op_sel_hi:[1,0]
	v_pk_mul_f32 v[96:97], v[96:97], s[2:3] op_sel_hi:[1,0]
	v_pk_mul_f32 v[94:95], v[94:95], s[2:3] op_sel_hi:[1,0]
	v_pk_mul_f32 v[92:93], v[92:93], s[2:3] op_sel_hi:[1,0]
	v_pk_mul_f32 v[90:91], v[90:91], s[2:3] op_sel_hi:[1,0]
	v_pk_mul_f32 v[80:81], v[80:81], s[2:3] op_sel_hi:[1,0]
	v_pk_mul_f32 v[114:115], v[78:79], s[2:3] op_sel_hi:[1,0]
	v_pk_mul_f32 v[78:79], v[72:73], s[2:3] op_sel_hi:[1,0]
	v_pk_mul_f32 v[116:117], v[70:71], s[2:3] op_sel_hi:[1,0]
	v_pk_mul_f32 v[28:29], v[88:89], s[2:3] op_sel_hi:[1,0]
	v_pk_mul_f32 v[70:71], v[86:87], s[2:3] op_sel_hi:[1,0]
	v_pk_mul_f32 v[26:27], v[84:85], s[2:3] op_sel_hi:[1,0]
	v_pk_mul_f32 v[72:73], v[82:83], s[2:3] op_sel_hi:[1,0]
	v_pk_mul_f32 v[64:65], v[64:65], s[2:3] op_sel_hi:[1,0]
	v_pk_mul_f32 v[62:63], v[62:63], s[2:3] op_sel_hi:[1,0]
	v_pk_mul_f32 v[56:57], v[56:57], s[2:3] op_sel_hi:[1,0]
	v_pk_mul_f32 v[54:55], v[54:55], s[2:3] op_sel_hi:[1,0]
	v_pk_mul_f32 v[12:13], v[76:77], s[2:3] op_sel_hi:[1,0]
	v_pk_mul_f32 v[18:19], v[74:75], s[2:3] op_sel_hi:[1,0]
	v_pk_mul_f32 v[10:11], v[68:69], s[2:3] op_sel_hi:[1,0]
	v_pk_mul_f32 v[20:21], v[66:67], s[2:3] op_sel_hi:[1,0]
	v_pk_mul_f32 v[32:33], v[48:49], s[2:3] op_sel_hi:[1,0]
	v_pk_mul_f32 v[46:47], v[46:47], s[2:3] op_sel_hi:[1,0]
	v_pk_mul_f32 v[30:31], v[44:45], s[2:3] op_sel_hi:[1,0]
	v_pk_mul_f32 v[42:43], v[42:43], s[2:3] op_sel_hi:[1,0]
	v_pk_mul_f32 v[4:5], v[60:61], s[2:3] op_sel_hi:[1,0]
	v_pk_mul_f32 v[6:7], v[58:59], s[2:3] op_sel_hi:[1,0]
	v_pk_mul_f32 v[2:3], v[52:53], s[2:3] op_sel_hi:[1,0]
	v_pk_mul_f32 v[8:9], v[50:51], s[2:3] op_sel_hi:[1,0]
	v_pk_mul_f32 v[16:17], v[40:41], s[2:3] op_sel_hi:[1,0]
	v_pk_mul_f32 v[22:23], v[38:39], s[2:3] op_sel_hi:[1,0]
	v_pk_mul_f32 v[14:15], v[36:37], s[2:3] op_sel_hi:[1,0]
	v_pk_mul_f32 v[24:25], v[34:35], s[2:3] op_sel_hi:[1,0]
